# nt weight stores + K-loop placement: gate/up +40B, both in-projections and out-projection headers on a 64-byte boundary
# speedup vs baseline: 1.0042x; 1.0042x over previous
; #define LAS __attribute__((address_space(3)))
; #define G8_STAGE(bufoff, gbase, voff) do { _Pragma("unroll") for (int _i = 0; _i < 2; ++_i) \
;         __builtin_amdgcn_global_load_lds((const unsigned*)((const char*)(gbase) + (voff)[_i]), (LAS unsigned*)(lds + (bufoff) + ldsw + _i * 8192), 16, 0, 0); } while (0)
; #define G8_WAIT_L(n) asm volatile("s_waitcnt lgkmcnt(" #n ")" ::: "memory")
; #define G8_BAR __builtin_amdgcn_s_barrier()
; #define G8_SCHED __builtin_amdgcn_sched_barrier(0)
; template <class Epi, class Sched>
; __device__ __forceinline__ void gemm_phase(LAS unsigned char* lds, const int K, const Sched& S, const Epi& E) {
;     ...
;         const bool has_next = S.next(ui + 1, nxt);
;         const char* nA = has_next ? nxt.A : cA; const char* nB = has_next ? nxt.B : cB;
; #pragma unroll 1
;         for (int t = 0; t < nt; t += 2) {
;             const bool last = (t == nt - 2);
;             const char* a1 = cA + (size_t)(t + 1) * kstep;
;             const char* a2 = last ? nA : cA + (size_t)(t + 2) * kstep; const char* b2 = last ? nB : cB + (size_t)(t + 2) * kstep;
;             const char* a3 = a2 + kstep; const char* b3 = b2 + kstep;
;             G8_LDB(B0, 0, 0); G8_SCHED; G8_LDA(At, 0, 0); G8_STAGE(G8_SA(1, 1), a1, oc[1]);
;             if (last && has_next) S.aoff(nxt, tid, oc);
;             G8_WAIT_L(8); G8_BAR; G8_WAIT_L(0); G8_MMA(0, 0, At, B0); G8_BAR; G8_SCHED;
;             G8_LDB(B1, 0, 1); G8_STAGE(G8_SB(0, 0), b2, voffB);
;             G8_BAR; G8_WAIT_L(0); G8_MMA(0, 1, At, B1); G8_BAR;
;             G8_LDA(At, 0, 1); G8_STAGE(G8_SA(0, 0), a2, oc[0]);
;             G8_BAR; G8_WAIT_L(0); G8_MMA(1, 0, At, B0); G8_BAR; G8_SCHED;
;     __device__ __forceinline__ void init(f32x4 (&acc)[2][2][4][2], const g8::Unit& u, int wc, int fq) const {
;         const int colp = u.pn * 256 + wc * 32 + fq * 8;
; #pragma unroll
;         for (int b = 0; b < 2; ++b)
; #pragma unroll
;             for (int n = 0; n < 2; ++n) { const u32x2 bw = *(const LAS u32x2*)(biasL + colp + b * 128 + 4 * n);
;                 const f32x4 bv = (f32x4){__uint_as_float(bw[0] << 16), __uint_as_float(bw[0] & 0xffff0000u), __uint_as_float(bw[1] << 16), __uint_as_float(bw[1] & 0xffff0000u)};
; #pragma unroll
;                 for (int a = 0; a < 2; ++a)
; #pragma unroll
;                     for (int m = 0; m < 4; ++m) acc[a][b][m][n] = bv; } }
.LBB0_319:
	v_mov_b64_e32 v[18:19], 0x480
	v_cmp_lt_i64_e64 s[34:35], s[34:35], v[18:19]
	s_add_u32 s5, s36, 0x100
	v_mov_b64_e32 v[20:21], v[4:5]
	v_mov_b64_e32 v[24:25], v[8:9]
	v_mov_b64_e32 v[36:37], v[4:5]
	v_mov_b64_e32 v[40:41], v[8:9]
	v_mov_b64_e32 v[52:53], v[4:5]
	v_mov_b64_e32 v[56:57], v[8:9]
	v_mov_b64_e32 v[28:29], v[12:13]
	v_mov_b64_e32 v[32:33], v[16:17]
	v_mov_b64_e32 v[44:45], v[12:13]
	v_mov_b64_e32 v[48:49], v[16:17]
	v_mov_b64_e32 v[60:61], v[12:13]
	v_mov_b64_e32 v[64:65], v[16:17]
	v_mov_b64_e32 v[68:69], v[4:5]
	v_mov_b64_e32 v[72:73], v[8:9]
	v_mov_b64_e32 v[84:85], v[4:5]
	v_mov_b64_e32 v[88:89], v[8:9]
	v_mov_b64_e32 v[100:101], v[4:5]
	v_mov_b64_e32 v[104:105], v[8:9]
	v_mov_b64_e32 v[116:117], v[4:5]
	v_mov_b64_e32 v[120:121], v[8:9]
	v_mov_b64_e32 v[76:77], v[12:13]
	v_mov_b64_e32 v[80:81], v[16:17]
	v_mov_b64_e32 v[92:93], v[12:13]
	v_mov_b64_e32 v[96:97], v[16:17]
	v_mov_b64_e32 v[108:109], v[12:13]
	v_mov_b64_e32 v[112:113], v[16:17]
	v_mov_b64_e32 v[124:125], v[12:13]
	v_mov_b64_e32 v[128:129], v[16:17]
	s_addc_u32 s9, s37, 0
	s_mov_b32 s11, -2
	v_mov_b64_e32 v[18:19], v[2:3]
	v_mov_b64_e32 v[22:23], v[6:7]
	v_mov_b64_e32 v[34:35], v[2:3]
	v_mov_b64_e32 v[38:39], v[6:7]
	v_mov_b64_e32 v[50:51], v[2:3]
	v_mov_b64_e32 v[54:55], v[6:7]
	v_mov_b64_e32 v[26:27], v[10:11]
	v_mov_b64_e32 v[30:31], v[14:15]
	v_mov_b64_e32 v[42:43], v[10:11]
	v_mov_b64_e32 v[46:47], v[14:15]
	v_mov_b64_e32 v[58:59], v[10:11]
	v_mov_b64_e32 v[62:63], v[14:15]
	v_mov_b64_e32 v[66:67], v[2:3]
	v_mov_b64_e32 v[70:71], v[6:7]
	v_mov_b64_e32 v[82:83], v[2:3]
	v_mov_b64_e32 v[86:87], v[6:7]
	v_mov_b64_e32 v[98:99], v[2:3]
	v_mov_b64_e32 v[102:103], v[6:7]
	v_mov_b64_e32 v[114:115], v[2:3]
	v_mov_b64_e32 v[118:119], v[6:7]
	v_mov_b64_e32 v[74:75], v[10:11]
	v_mov_b64_e32 v[78:79], v[14:15]
	v_mov_b64_e32 v[90:91], v[10:11]
	v_mov_b64_e32 v[94:95], v[14:15]
	v_mov_b64_e32 v[106:107], v[10:11]
	v_mov_b64_e32 v[110:111], v[14:15]
	v_mov_b64_e32 v[122:123], v[10:11]
	v_mov_b64_e32 v[126:127], v[14:15]
	s_nop 0
	s_nop 0
	s_nop 0
	s_nop 0
	s_nop 0
	s_nop 0
	s_nop 0
.LBB0_320:
	s_add_u32 s36, s2, 0x100
	s_addc_u32 s37, s3, 0
	s_add_i32 s82, 0, 0x10000
	v_add_u32_e32 v0, s82, v145
	ds_read_b128 v[154:157], v0
	ds_read_b128 v[158:161], v0 offset:1024
	ds_read_b128 v[162:165], v0 offset:2048
	ds_read_b128 v[166:169], v0 offset:3072
	s_cmp_eq_u32 s11, 12
	s_cselect_b32 s49, s43, s37
	s_cselect_b32 s48, s42, s36
	s_cselect_b32 s47, s45, s9
	s_cselect_b32 s46, s44, s5
	v_lshl_add_u64 v[150:151], s[2:3], 0, v[148:149]
	s_add_i32 m0, s58, 0xc000
	ds_read_b128 v[170:173], v153
	ds_read_b128 v[174:177], v153 offset:1024
	ds_read_b128 v[178:181], v153 offset:2048
	ds_read_b128 v[182:185], v153 offset:3072
	ds_read_b128 v[186:189], v153 offset:4096
	ds_read_b128 v[190:193], v153 offset:5120
	ds_read_b128 v[194:197], v153 offset:6144
	ds_read_b128 v[198:201], v153 offset:7168
	global_load_lds_dwordx4 v[150:151], off
	v_lshl_add_u64 v[150:151], s[2:3], 0, v[146:147]
	s_add_i32 m0, s58, 0xe000
	s_nop 0
	global_load_lds_dwordx4 v[150:151], off
	s_waitcnt lgkmcnt(8)
	s_barrier
	s_waitcnt lgkmcnt(0)
	s_setprio 1
	s_waitcnt lgkmcnt(0)
	v_mfma_f32_16x16x32_bf16 v[126:129], v[154:157], v[170:173], v[126:129]
	v_mfma_f32_16x16x32_bf16 v[122:125], v[162:165], v[170:173], v[122:125]
	v_mfma_f32_16x16x32_bf16 v[110:113], v[154:157], v[178:181], v[110:113]
	v_mfma_f32_16x16x32_bf16 v[106:109], v[162:165], v[178:181], v[106:109]
	v_mfma_f32_16x16x32_bf16 v[94:97], v[154:157], v[186:189], v[94:97]
	v_mfma_f32_16x16x32_bf16 v[90:93], v[162:165], v[186:189], v[90:93]
	v_mfma_f32_16x16x32_bf16 v[78:81], v[154:157], v[194:197], v[78:81]
	v_mfma_f32_16x16x32_bf16 v[74:77], v[162:165], v[194:197], v[74:77]
	v_mfma_f32_16x16x32_bf16 v[126:129], v[158:161], v[174:177], v[126:129]
	v_mfma_f32_16x16x32_bf16 v[122:125], v[166:169], v[174:177], v[122:125]
	v_mfma_f32_16x16x32_bf16 v[110:113], v[158:161], v[182:185], v[110:113]
	v_mfma_f32_16x16x32_bf16 v[106:109], v[166:169], v[182:185], v[106:109]
	v_mfma_f32_16x16x32_bf16 v[94:97], v[158:161], v[190:193], v[94:97]
	v_mfma_f32_16x16x32_bf16 v[90:93], v[166:169], v[190:193], v[90:93]
	v_mfma_f32_16x16x32_bf16 v[78:81], v[158:161], v[198:201], v[78:81]
	v_mfma_f32_16x16x32_bf16 v[74:77], v[166:169], v[198:201], v[74:77]
	s_setprio 0
	s_barrier
	s_add_i32 s83, 0, 0x14000
	s_add_i32 s2, s82, s57
	v_add_u32_e32 v0, s83, v145
	v_lshl_add_u64 v[150:151], s[46:47], 0, v[132:133]
	s_mov_b32 m0, s2
	ds_read_b128 v[216:219], v0
	ds_read_b128 v[220:223], v0 offset:1024
	ds_read_b128 v[224:227], v0 offset:2048
	ds_read_b128 v[228:231], v0 offset:3072
	global_load_lds_dwordx4 v[150:151], off
	v_lshl_add_u64 v[232:233], s[46:47], 0, v[134:135]
	s_add_i32 m0, s2, 0x2000
	s_nop 0
	global_load_lds_dwordx4 v[232:233], off
	s_barrier
	s_waitcnt lgkmcnt(0)
	s_setprio 1
	s_waitcnt lgkmcnt(0)
	v_mfma_f32_16x16x32_bf16 v[118:121], v[216:219], v[170:173], v[118:121]
	v_mfma_f32_16x16x32_bf16 v[114:117], v[224:227], v[170:173], v[114:117]
	v_mfma_f32_16x16x32_bf16 v[102:105], v[216:219], v[178:181], v[102:105]
	v_mfma_f32_16x16x32_bf16 v[98:101], v[224:227], v[178:181], v[98:101]
	v_mfma_f32_16x16x32_bf16 v[86:89], v[216:219], v[186:189], v[86:89]
	v_mfma_f32_16x16x32_bf16 v[82:85], v[224:227], v[186:189], v[82:85]
	v_mfma_f32_16x16x32_bf16 v[70:73], v[216:219], v[194:197], v[70:73]
	v_mfma_f32_16x16x32_bf16 v[66:69], v[224:227], v[194:197], v[66:69]
	v_mfma_f32_16x16x32_bf16 v[118:121], v[220:223], v[174:177], v[118:121]
	v_mfma_f32_16x16x32_bf16 v[114:117], v[228:231], v[174:177], v[114:117]
	v_mfma_f32_16x16x32_bf16 v[102:105], v[220:223], v[182:185], v[102:105]
	v_mfma_f32_16x16x32_bf16 v[98:101], v[228:231], v[182:185], v[98:101]
	v_mfma_f32_16x16x32_bf16 v[86:89], v[220:223], v[190:193], v[86:89]
	v_mfma_f32_16x16x32_bf16 v[82:85], v[228:231], v[190:193], v[82:85]
	v_mfma_f32_16x16x32_bf16 v[70:73], v[220:223], v[198:201], v[70:73]
	v_mfma_f32_16x16x32_bf16 v[66:69], v[228:231], v[198:201], v[66:69]
	s_setprio 0
	s_mov_b32 m0, s58
	v_lshl_add_u64 v[234:235], s[48:49], 0, v[136:137]
	s_barrier
; #define G8_STAGE(bufoff, gbase, voff) do { _Pragma("unroll") for (int _i = 0; _i < 2; ++_i) \
;         __builtin_amdgcn_global_load_lds((const unsigned*)((const char*)(gbase) + (voff)[_i]), (LAS unsigned*)(lds + (bufoff) + ldsw + _i * 8192), 16, 0, 0); } while (0)
; #define G8_LDA(dst, b, h) do { _Pragma("unroll") for (int m = 0; m < 4; ++m) _Pragma("unroll") for (int k = 0; k < 2; ++k) dst[m][k] = *(const LAS bf16x8*)(lds + G8_SA(b, h) + aoff + m * 2048 + k * 1024); } while (0)
; #define G8_LDB(dst, b, h) do { _Pragma("unroll") for (int n = 0; n < 2; ++n) _Pragma("unroll") for (int k = 0; k < 2; ++k) dst[n][k] = *(const LAS bf16x8*)(lds + G8_SB(b, h) + boff + n * 2048 + k * 1024); } while (0)
; #define G8_MMA(ai, bj, At, Bt) do { __builtin_amdgcn_s_setprio(1); _Pragma("unroll") for (int m = 0; m < 4; ++m) _Pragma("unroll") for (int n = 0; n < 2; ++n) _Pragma("unroll") for (int k = 0; k < 2; ++k) \
;         acc[ai][bj][m][n] = __builtin_amdgcn_mfma_f32_16x16x32_bf16(Bt[n][k], At[m][k], acc[ai][bj][m][n], 0, 0, 0); __builtin_amdgcn_s_setprio(0); } while (0)
; #define G8_WAIT_V(n) asm volatile("s_waitcnt vmcnt(" #n ")" ::: "memory")
; #define G8_WAIT_L(n) asm volatile("s_waitcnt lgkmcnt(" #n ")" ::: "memory")
; #define G8_BAR __builtin_amdgcn_s_barrier()
; #define G8_SCHED __builtin_amdgcn_sched_barrier(0)
; template <class Epi, class Sched>
; __device__ __forceinline__ void gemm_phase(LAS unsigned char* lds, const int K, const Sched& S, const Epi& E) {
;     ...
;             G8_LDA(At, 0, 1); G8_STAGE(G8_SA(0, 0), a2, oc[0]);
;             G8_BAR; G8_WAIT_L(0); G8_MMA(1, 0, At, B0); G8_BAR; G8_SCHED;
;             G8_STAGE(G8_SB(0, 1), b2 + hstep, voffB);
;             G8_WAIT_V(6); G8_BAR; G8_MMA(1, 1, At, B1); G8_BAR;
;             G8_LDB(B0, 1, 0); G8_SCHED; G8_LDA(At, 1, 0); G8_STAGE(G8_SA(0, 1), a2, oc[1]);
;             G8_WAIT_L(8); G8_BAR; G8_WAIT_L(0); G8_MMA(0, 0, At, B0); G8_BAR; G8_SCHED;
;             G8_LDB(B1, 1, 1); G8_STAGE(G8_SB(1, 0), b3, voffB);
	ds_read_b128 v[170:173], v153 offset:16384
	ds_read_b128 v[174:177], v153 offset:17408
	ds_read_b128 v[178:181], v153 offset:18432
	ds_read_b128 v[182:185], v153 offset:19456
	ds_read_b128 v[186:189], v153 offset:20480
	ds_read_b128 v[190:193], v153 offset:21504
	ds_read_b128 v[194:197], v153 offset:22528
	ds_read_b128 v[198:201], v153 offset:23552
	global_load_lds_dwordx4 v[234:235], off
	v_lshl_add_u64 v[236:237], s[48:49], 0, v[140:141]
	s_mov_b32 m0, s59
	s_nop 0
	global_load_lds_dwordx4 v[236:237], off
	s_barrier
	s_waitcnt lgkmcnt(0)
	s_setprio 1
	s_waitcnt lgkmcnt(0)
	v_mfma_f32_16x16x32_bf16 v[62:65], v[154:157], v[170:173], v[62:65]
	v_mfma_f32_16x16x32_bf16 v[58:61], v[162:165], v[170:173], v[58:61]
	v_mfma_f32_16x16x32_bf16 v[46:49], v[154:157], v[178:181], v[46:49]
	v_mfma_f32_16x16x32_bf16 v[42:45], v[162:165], v[178:181], v[42:45]
	v_mfma_f32_16x16x32_bf16 v[30:33], v[154:157], v[186:189], v[30:33]
	v_mfma_f32_16x16x32_bf16 v[26:29], v[162:165], v[186:189], v[26:29]
	v_mfma_f32_16x16x32_bf16 v[14:17], v[154:157], v[194:197], v[14:17]
	v_mfma_f32_16x16x32_bf16 v[10:13], v[162:165], v[194:197], v[10:13]
	v_mfma_f32_16x16x32_bf16 v[62:65], v[158:161], v[174:177], v[62:65]
	v_mfma_f32_16x16x32_bf16 v[58:61], v[166:169], v[174:177], v[58:61]
	v_mfma_f32_16x16x32_bf16 v[46:49], v[158:161], v[182:185], v[46:49]
	v_mfma_f32_16x16x32_bf16 v[42:45], v[166:169], v[182:185], v[42:45]
	v_mfma_f32_16x16x32_bf16 v[30:33], v[158:161], v[190:193], v[30:33]
	v_mfma_f32_16x16x32_bf16 v[26:29], v[166:169], v[190:193], v[26:29]
	v_mfma_f32_16x16x32_bf16 v[14:17], v[158:161], v[198:201], v[14:17]
	v_mfma_f32_16x16x32_bf16 v[10:13], v[166:169], v[198:201], v[10:13]
	s_setprio 0
	s_barrier
	s_add_u32 s2, s46, 0x40000
	s_addc_u32 s3, s47, 0
	s_add_i32 s82, s83, s57
	v_lshl_add_u64 v[154:155], s[2:3], 0, v[132:133]
	s_mov_b32 m0, s82
	s_nop 0
	global_load_lds_dwordx4 v[154:155], off
	v_lshl_add_u64 v[154:155], s[2:3], 0, v[134:135]
	s_add_i32 m0, s82, 0x2000
	s_nop 0
	global_load_lds_dwordx4 v[154:155], off
	s_waitcnt vmcnt(6)
	s_barrier
	s_setprio 1
	v_mfma_f32_16x16x32_bf16 v[54:57], v[216:219], v[170:173], v[54:57]
	v_mfma_f32_16x16x32_bf16 v[50:53], v[224:227], v[170:173], v[50:53]
	v_mfma_f32_16x16x32_bf16 v[38:41], v[216:219], v[178:181], v[38:41]
	v_mfma_f32_16x16x32_bf16 v[34:37], v[224:227], v[178:181], v[34:37]
	v_mfma_f32_16x16x32_bf16 v[22:25], v[216:219], v[186:189], v[22:25]
	v_mfma_f32_16x16x32_bf16 v[18:21], v[224:227], v[186:189], v[18:21]
	v_mfma_f32_16x16x32_bf16 v[6:9], v[216:219], v[194:197], v[6:9]
	v_mfma_f32_16x16x32_bf16 v[2:5], v[224:227], v[194:197], v[2:5]
	v_mfma_f32_16x16x32_bf16 v[54:57], v[220:223], v[174:177], v[54:57]
	v_mfma_f32_16x16x32_bf16 v[50:53], v[228:231], v[174:177], v[50:53]
	v_mfma_f32_16x16x32_bf16 v[38:41], v[220:223], v[182:185], v[38:41]
	v_mfma_f32_16x16x32_bf16 v[34:37], v[228:231], v[182:185], v[34:37]
	v_mfma_f32_16x16x32_bf16 v[22:25], v[220:223], v[190:193], v[22:25]
	v_mfma_f32_16x16x32_bf16 v[18:21], v[228:231], v[190:193], v[18:21]
	v_mfma_f32_16x16x32_bf16 v[6:9], v[220:223], v[198:201], v[6:9]
	v_mfma_f32_16x16x32_bf16 v[2:5], v[228:231], v[198:201], v[2:5]
	s_setprio 0
	s_add_i32 s2, 0, 0x18000
	v_add_u32_e32 v0, s2, v145
	s_barrier
	ds_read_b128 v[154:157], v0
	ds_read_b128 v[158:161], v0 offset:1024
	ds_read_b128 v[162:165], v0 offset:2048
	ds_read_b128 v[166:169], v0 offset:3072
	s_mov_b32 m0, s60
	v_lshl_add_u64 v[216:217], s[48:49], 0, v[138:139]
	ds_read_b128 v[170:173], v153 offset:32768
	ds_read_b128 v[174:177], v153 offset:33792
	ds_read_b128 v[178:181], v153 offset:34816
	ds_read_b128 v[182:185], v153 offset:35840
	ds_read_b128 v[186:189], v153 offset:36864
	ds_read_b128 v[190:193], v153 offset:37888
	ds_read_b128 v[194:197], v153 offset:38912
	ds_read_b128 v[198:201], v153 offset:39936
	global_load_lds_dwordx4 v[216:217], off
	v_lshl_add_u64 v[216:217], s[48:49], 0, v[142:143]
	s_mov_b32 m0, s61
	s_nop 0
	global_load_lds_dwordx4 v[216:217], off
	s_waitcnt lgkmcnt(8)
	s_barrier
	s_waitcnt lgkmcnt(0)
	s_setprio 1
	s_waitcnt lgkmcnt(0)
	v_mfma_f32_16x16x32_bf16 v[126:129], v[154:157], v[170:173], v[126:129]
	v_mfma_f32_16x16x32_bf16 v[122:125], v[162:165], v[170:173], v[122:125]
	v_mfma_f32_16x16x32_bf16 v[110:113], v[154:157], v[178:181], v[110:113]
	v_mfma_f32_16x16x32_bf16 v[106:109], v[162:165], v[178:181], v[106:109]
	v_mfma_f32_16x16x32_bf16 v[94:97], v[154:157], v[186:189], v[94:97]
	v_mfma_f32_16x16x32_bf16 v[90:93], v[162:165], v[186:189], v[90:93]
	v_mfma_f32_16x16x32_bf16 v[78:81], v[154:157], v[194:197], v[78:81]
	v_mfma_f32_16x16x32_bf16 v[74:77], v[162:165], v[194:197], v[74:77]
	v_mfma_f32_16x16x32_bf16 v[126:129], v[158:161], v[174:177], v[126:129]
	v_mfma_f32_16x16x32_bf16 v[122:125], v[166:169], v[174:177], v[122:125]
	v_mfma_f32_16x16x32_bf16 v[110:113], v[158:161], v[182:185], v[110:113]
	v_mfma_f32_16x16x32_bf16 v[106:109], v[166:169], v[182:185], v[106:109]
	v_mfma_f32_16x16x32_bf16 v[94:97], v[158:161], v[190:193], v[94:97]
	v_mfma_f32_16x16x32_bf16 v[90:93], v[166:169], v[190:193], v[90:93]
	v_mfma_f32_16x16x32_bf16 v[78:81], v[158:161], v[198:201], v[78:81]
	v_mfma_f32_16x16x32_bf16 v[74:77], v[166:169], v[198:201], v[74:77]
	s_setprio 0
	s_barrier
	s_add_i32 s48, 0, 0x1c000
	s_add_i32 s2, s2, s57
	v_add_u32_e32 v0, s48, v145
	v_lshl_add_u64 v[150:151], v[150:151], 0, s[18:19]
	s_mov_b32 m0, s2
	ds_read_b128 v[216:219], v0
	ds_read_b128 v[220:223], v0 offset:1024
	ds_read_b128 v[224:227], v0 offset:2048
	ds_read_b128 v[228:231], v0 offset:3072
	global_load_lds_dwordx4 v[150:151], off
	v_lshl_add_u64 v[150:151], v[232:233], 0, s[18:19]
	s_add_i32 m0, s2, 0x2000
	s_nop 0
	global_load_lds_dwordx4 v[150:151], off
	s_barrier
; #define G8_STAGE(bufoff, gbase, voff) do { _Pragma("unroll") for (int _i = 0; _i < 2; ++_i) \
;         __builtin_amdgcn_global_load_lds((const unsigned*)((const char*)(gbase) + (voff)[_i]), (LAS unsigned*)(lds + (bufoff) + ldsw + _i * 8192), 16, 0, 0); } while (0)
; #define G8_LDA(dst, b, h) do { _Pragma("unroll") for (int m = 0; m < 4; ++m) _Pragma("unroll") for (int k = 0; k < 2; ++k) dst[m][k] = *(const LAS bf16x8*)(lds + G8_SA(b, h) + aoff + m * 2048 + k * 1024); } while (0)
; #define G8_LDB(dst, b, h) do { _Pragma("unroll") for (int n = 0; n < 2; ++n) _Pragma("unroll") for (int k = 0; k < 2; ++k) dst[n][k] = *(const LAS bf16x8*)(lds + G8_SB(b, h) + boff + n * 2048 + k * 1024); } while (0)
; #define G8_MMA(ai, bj, At, Bt) do { __builtin_amdgcn_s_setprio(1); _Pragma("unroll") for (int m = 0; m < 4; ++m) _Pragma("unroll") for (int n = 0; n < 2; ++n) _Pragma("unroll") for (int k = 0; k < 2; ++k) \
;         acc[ai][bj][m][n] = __builtin_amdgcn_mfma_f32_16x16x32_bf16(Bt[n][k], At[m][k], acc[ai][bj][m][n], 0, 0, 0); __builtin_amdgcn_s_setprio(0); } while (0)
; #define G8_WAIT_V(n) asm volatile("s_waitcnt vmcnt(" #n ")" ::: "memory")
; #define G8_WAIT_L(n) asm volatile("s_waitcnt lgkmcnt(" #n ")" ::: "memory")
; #define G8_BAR __builtin_amdgcn_s_barrier()
; #define G8_SCHED __builtin_amdgcn_sched_barrier(0)
; __device__ __forceinline__ f32x4 gelu4(const f32x4 x) {
;     const f32x4 t = x * ((x * x) * (-0.10294323886f) + (-2.30220819813f)); f32x4 d;
; #pragma unroll
;     for (int e = 0; e < 4; ++e) d[e] = __builtin_amdgcn_exp2f(t[e]);
;     d = d + 1.f;
; #pragma unroll
;     for (int e = 0; e < 4; ++e) d[e] = __builtin_amdgcn_rcpf(d[e]);
;     return x * d; }
; template <class Epi, class Sched>
; __device__ __forceinline__ void gemm_phase(LAS unsigned char* lds, const int K, const Sched& S, const Epi& E) {
;     ...
;             G8_WAIT_L(8); G8_BAR; G8_WAIT_L(0); G8_MMA(0, 0, At, B0); G8_BAR; G8_SCHED;
;             G8_LDB(B1, 1, 1); G8_STAGE(G8_SB(1, 0), b3, voffB);
;             G8_BAR; G8_WAIT_L(0); G8_MMA(0, 1, At, B1); G8_BAR;
;             G8_LDA(At, 1, 1); G8_STAGE(G8_SA(1, 0), a3, oc[0]);
;             G8_BAR; G8_WAIT_L(0); G8_MMA(1, 0, At, B0); G8_BAR; G8_SCHED;
;             G8_STAGE(G8_SB(1, 1), b3 + hstep, voffB);
;             G8_WAIT_V(6); G8_BAR; G8_MMA(1, 1, At, B1); G8_BAR;
;         }
	s_waitcnt lgkmcnt(0)
	s_setprio 1
	s_waitcnt lgkmcnt(0)
	v_mfma_f32_16x16x32_bf16 v[118:121], v[216:219], v[170:173], v[118:121]
	v_mfma_f32_16x16x32_bf16 v[114:117], v[224:227], v[170:173], v[114:117]
	v_mfma_f32_16x16x32_bf16 v[102:105], v[216:219], v[178:181], v[102:105]
	v_mfma_f32_16x16x32_bf16 v[98:101], v[224:227], v[178:181], v[98:101]
	v_mfma_f32_16x16x32_bf16 v[86:89], v[216:219], v[186:189], v[86:89]
	v_mfma_f32_16x16x32_bf16 v[82:85], v[224:227], v[186:189], v[82:85]
	v_mfma_f32_16x16x32_bf16 v[70:73], v[216:219], v[194:197], v[70:73]
	v_mfma_f32_16x16x32_bf16 v[66:69], v[224:227], v[194:197], v[66:69]
	v_mfma_f32_16x16x32_bf16 v[118:121], v[220:223], v[174:177], v[118:121]
	v_mfma_f32_16x16x32_bf16 v[114:117], v[228:231], v[174:177], v[114:117]
	v_mfma_f32_16x16x32_bf16 v[102:105], v[220:223], v[182:185], v[102:105]
	v_mfma_f32_16x16x32_bf16 v[98:101], v[228:231], v[182:185], v[98:101]
	v_mfma_f32_16x16x32_bf16 v[86:89], v[220:223], v[190:193], v[86:89]
	v_mfma_f32_16x16x32_bf16 v[82:85], v[228:231], v[190:193], v[82:85]
	v_mfma_f32_16x16x32_bf16 v[70:73], v[220:223], v[198:201], v[70:73]
	v_mfma_f32_16x16x32_bf16 v[66:69], v[228:231], v[198:201], v[66:69]
	s_setprio 0
	s_mov_b32 m0, s64
	v_lshl_add_u64 v[150:151], v[234:235], 0, s[18:19]
	s_barrier
	ds_read_b128 v[170:173], v153 offset:49152
	ds_read_b128 v[174:177], v153 offset:50176
	ds_read_b128 v[178:181], v153 offset:51200
	ds_read_b128 v[182:185], v153 offset:52224
	ds_read_b128 v[186:189], v153 offset:53248
	ds_read_b128 v[190:193], v153 offset:54272
	ds_read_b128 v[194:197], v153 offset:55296
	ds_read_b128 v[198:201], v153 offset:56320
	global_load_lds_dwordx4 v[150:151], off
	v_lshl_add_u64 v[150:151], v[236:237], 0, s[18:19]
	s_mov_b32 m0, s65
	s_nop 0
	global_load_lds_dwordx4 v[150:151], off
	s_barrier
	s_waitcnt lgkmcnt(0)
	s_setprio 1
	s_waitcnt lgkmcnt(0)
	v_mfma_f32_16x16x32_bf16 v[62:65], v[154:157], v[170:173], v[62:65]
	v_mfma_f32_16x16x32_bf16 v[58:61], v[162:165], v[170:173], v[58:61]
	v_mfma_f32_16x16x32_bf16 v[46:49], v[154:157], v[178:181], v[46:49]
	v_mfma_f32_16x16x32_bf16 v[42:45], v[162:165], v[178:181], v[42:45]
	v_mfma_f32_16x16x32_bf16 v[30:33], v[154:157], v[186:189], v[30:33]
	v_mfma_f32_16x16x32_bf16 v[26:29], v[162:165], v[186:189], v[26:29]
	v_mfma_f32_16x16x32_bf16 v[14:17], v[154:157], v[194:197], v[14:17]
	v_mfma_f32_16x16x32_bf16 v[10:13], v[162:165], v[194:197], v[10:13]
	v_mfma_f32_16x16x32_bf16 v[62:65], v[158:161], v[174:177], v[62:65]
	v_mfma_f32_16x16x32_bf16 v[58:61], v[166:169], v[174:177], v[58:61]
	v_mfma_f32_16x16x32_bf16 v[46:49], v[158:161], v[182:185], v[46:49]
	v_mfma_f32_16x16x32_bf16 v[42:45], v[166:169], v[182:185], v[42:45]
	v_mfma_f32_16x16x32_bf16 v[30:33], v[158:161], v[190:193], v[30:33]
	v_mfma_f32_16x16x32_bf16 v[26:29], v[166:169], v[190:193], v[26:29]
	v_mfma_f32_16x16x32_bf16 v[14:17], v[158:161], v[198:201], v[14:17]
	v_mfma_f32_16x16x32_bf16 v[10:13], v[166:169], v[198:201], v[10:13]
	s_setprio 0
	s_barrier
	s_add_u32 s2, s46, 0x40080
	s_addc_u32 s3, s47, 0
	s_add_i32 s46, s48, s57
	v_lshl_add_u64 v[150:151], s[2:3], 0, v[132:133]
	s_mov_b32 m0, s46
	s_nop 0
	global_load_lds_dwordx4 v[150:151], off
	v_lshl_add_u64 v[150:151], s[2:3], 0, v[134:135]
	s_add_i32 m0, s46, 0x2000
	s_nop 0
	global_load_lds_dwordx4 v[150:151], off
	s_waitcnt vmcnt(6)
	s_barrier
	s_setprio 1
	v_mfma_f32_16x16x32_bf16 v[54:57], v[216:219], v[170:173], v[54:57]
	v_mfma_f32_16x16x32_bf16 v[50:53], v[224:227], v[170:173], v[50:53]
	v_mfma_f32_16x16x32_bf16 v[38:41], v[216:219], v[178:181], v[38:41]
	v_mfma_f32_16x16x32_bf16 v[34:37], v[224:227], v[178:181], v[34:37]
	v_mfma_f32_16x16x32_bf16 v[22:25], v[216:219], v[186:189], v[22:25]
	v_mfma_f32_16x16x32_bf16 v[18:21], v[224:227], v[186:189], v[18:21]
	v_mfma_f32_16x16x32_bf16 v[6:9], v[216:219], v[194:197], v[6:9]
	v_mfma_f32_16x16x32_bf16 v[2:5], v[224:227], v[194:197], v[2:5]
	v_mfma_f32_16x16x32_bf16 v[54:57], v[220:223], v[174:177], v[54:57]
	v_mfma_f32_16x16x32_bf16 v[50:53], v[228:231], v[174:177], v[50:53]
	v_mfma_f32_16x16x32_bf16 v[38:41], v[220:223], v[182:185], v[38:41]
	v_mfma_f32_16x16x32_bf16 v[34:37], v[228:231], v[182:185], v[34:37]
	v_mfma_f32_16x16x32_bf16 v[22:25], v[220:223], v[190:193], v[22:25]
	v_mfma_f32_16x16x32_bf16 v[18:21], v[228:231], v[190:193], v[18:21]
	v_mfma_f32_16x16x32_bf16 v[6:9], v[220:223], v[198:201], v[6:9]
	v_mfma_f32_16x16x32_bf16 v[2:5], v[228:231], v[198:201], v[2:5]
	s_setprio 0
	s_add_i32 s11, s11, 2
	s_add_u32 s5, s5, 0x100
	s_addc_u32 s9, s9, 0
	s_cmp_gt_u32 s11, 13
	s_mov_b64 s[2:3], s[36:37]
	s_barrier
	s_cbranch_scc0 .LBB0_320
	s_nop 0
	s_nop 0
	s_nop 0
	s_nop 0
	s_nop 0
	s_nop 0
	s_nop 0
	s_nop 0
	s_nop 0
	s_cmp_lt_i32 s14, 13
	s_cselect_b64 s[36:37], -1, 0
	s_and_b64 vcc, exec, s[36:37]
	s_cbranch_vccz .LBB0_325
	v_pk_mul_f32 v[154:155], v[126:127], v[126:127]
	v_pk_mul_f32 v[150:151], v[128:129], v[128:129]
	v_fmamk_f32 v0, v154, 0xbdd2d3e8, v202
	v_mul_f32_e32 v0, v126, v0
	v_exp_f32_e32 v154, v0
	v_fmamk_f32 v0, v155, 0xbdd2d3e8, v202
	v_mul_f32_e32 v0, v127, v0
	v_exp_f32_e32 v155, v0
	v_fmamk_f32 v0, v150, 0xbdd2d3e8, v202
	v_mul_f32_e32 v0, v128, v0
	v_exp_f32_e32 v150, v0
	v_fmamk_f32 v0, v151, 0xbdd2d3e8, v202
	v_mul_f32_e32 v0, v129, v0
	v_exp_f32_e32 v151, v0
	v_pk_add_f32 v[154:155], v[154:155], 1.0 op_sel_hi:[1,0]
	v_pk_add_f32 v[150:151], v[150:151], 1.0 op_sel_hi:[1,0]
	v_rcp_f32_e32 v154, v154
	v_rcp_f32_e32 v155, v155
	v_rcp_f32_e32 v150, v150
	v_rcp_f32_e32 v151, v151
	v_pk_mul_f32 v[126:127], v[126:127], v[154:155]
	v_pk_mul_f32 v[128:129], v[128:129], v[150:151]
	v_cndmask_b32_e64 v0, 0, 1, s[36:37]
	v_cmp_ne_u32_e64 s[2:3], 1, v0
	s_andn2_b64 vcc, exec, s[36:37]
	s_cbranch_vccz .LBB0_326

; #define G8_STAGE(bufoff, gbase, voff) do { _Pragma("unroll") for (int _i = 0; _i < 2; ++_i) \
;         __builtin_amdgcn_global_load_lds((const unsigned*)((const char*)(gbase) + (voff)[_i]), (LAS unsigned*)(lds + (bufoff) + ldsw + _i * 8192), 16, 0, 0); } while (0)
; #define G8_LDA(dst, b, h) do { _Pragma("unroll") for (int m = 0; m < 4; ++m) _Pragma("unroll") for (int k = 0; k < 2; ++k) dst[m][k] = *(const LAS bf16x8*)(lds + G8_SA(b, h) + aoff + m * 2048 + k * 1024); } while (0)
; #define G8_LDB(dst, b, h) do { _Pragma("unroll") for (int n = 0; n < 2; ++n) _Pragma("unroll") for (int k = 0; k < 2; ++k) dst[n][k] = *(const LAS bf16x8*)(lds + G8_SB(b, h) + boff + n * 2048 + k * 1024); } while (0)
; #define G8_MMA(ai, bj, At, Bt) do { __builtin_amdgcn_s_setprio(1); _Pragma("unroll") for (int m = 0; m < 4; ++m) _Pragma("unroll") for (int n = 0; n < 2; ++n) _Pragma("unroll") for (int k = 0; k < 2; ++k) \
;         acc[ai][bj][m][n] = __builtin_amdgcn_mfma_f32_16x16x32_bf16(Bt[n][k], At[m][k], acc[ai][bj][m][n], 0, 0, 0); __builtin_amdgcn_s_setprio(0); } while (0)
; #define G8_WAIT_L(n) asm volatile("s_waitcnt lgkmcnt(" #n ")" ::: "memory")
; #define G8_BAR __builtin_amdgcn_s_barrier()
; template <class Epi, class Sched>
; __device__ __forceinline__ void gemm_phase(LAS unsigned char* lds, const int K, const Sched& S, const Epi& E) {
;     ...
;         const bool has_next = S.next(ui + 1, nxt);
;         const char* nA = has_next ? nxt.A : cA; const char* nB = has_next ? nxt.B : cB;
; #pragma unroll 1
;         for (int t = 0; t < nt; t += 2) {
;             const bool last = (t == nt - 2);
;             const char* a1 = cA + (size_t)(t + 1) * kstep;
;             const char* a2 = last ? nA : cA + (size_t)(t + 2) * kstep; const char* b2 = last ? nB : cB + (size_t)(t + 2) * kstep;
;             const char* a3 = a2 + kstep; const char* b3 = b2 + kstep;
;             G8_LDB(B0, 0, 0); G8_SCHED; G8_LDA(At, 0, 0); G8_STAGE(G8_SA(1, 1), a1, oc[1]);
;             if (last && has_next) S.aoff(nxt, tid, oc);
;             G8_WAIT_L(8); G8_BAR; G8_WAIT_L(0); G8_MMA(0, 0, At, B0); G8_BAR; G8_SCHED;
;             G8_LDB(B1, 0, 1); G8_STAGE(G8_SB(0, 0), b2, voffB);
;             G8_BAR; G8_WAIT_L(0); G8_MMA(0, 1, At, B1); G8_BAR;
;             G8_LDA(At, 0, 1); G8_STAGE(G8_SA(0, 0), a2, oc[0]);
;             G8_BAR; G8_WAIT_L(0); G8_MMA(1, 0, At, B0); G8_BAR; G8_SCHED;
.LBB0_487:
	s_add_u32 s12, s0, 0x100
	s_addc_u32 s13, s1, 0
	s_add_i32 s49, 0, 0x10000
	v_add_u32_e32 v158, s49, v165
	ds_read_b128 v[130:133], v158
	ds_read_b128 v[134:137], v158 offset:1024
	ds_read_b128 v[154:157], v158 offset:2048
	ds_read_b128 v[158:161], v158 offset:3072
	s_cmp_eq_u32 s47, 12
	s_cselect_b32 s43, s23, s13
	s_cselect_b32 s42, s22, s12
	s_cselect_b32 s39, s37, s14
	s_cselect_b32 s38, s36, s3
	v_lshl_add_u64 v[162:163], s[0:1], 0, v[152:153]
	s_add_i32 m0, s76, 0xc000
	ds_read_b128 v[168:171], v167
	ds_read_b128 v[172:175], v167 offset:1024
	ds_read_b128 v[176:179], v167 offset:2048
	ds_read_b128 v[180:183], v167 offset:3072
	ds_read_b128 v[184:187], v167 offset:4096
	ds_read_b128 v[188:191], v167 offset:5120
	ds_read_b128 v[192:195], v167 offset:6144
	ds_read_b128 v[196:199], v167 offset:7168
	global_load_lds_dwordx4 v[162:163], off
	v_lshl_add_u64 v[162:163], s[0:1], 0, v[150:151]
	s_add_i32 m0, s76, 0xe000
	s_nop 0
	global_load_lds_dwordx4 v[162:163], off
	s_waitcnt lgkmcnt(8)
	s_barrier
	s_waitcnt lgkmcnt(0)
	s_setprio 1
	s_waitcnt lgkmcnt(0)
	v_mfma_f32_16x16x32_bf16 v[126:129], v[130:133], v[168:171], v[126:129]
	v_mfma_f32_16x16x32_bf16 v[118:121], v[154:157], v[168:171], v[118:121]
	v_mfma_f32_16x16x32_bf16 v[110:113], v[130:133], v[176:179], v[110:113]
	v_mfma_f32_16x16x32_bf16 v[102:105], v[154:157], v[176:179], v[102:105]
	v_mfma_f32_16x16x32_bf16 v[94:97], v[130:133], v[184:187], v[94:97]
	v_mfma_f32_16x16x32_bf16 v[86:89], v[154:157], v[184:187], v[86:89]
	v_mfma_f32_16x16x32_bf16 v[78:81], v[130:133], v[192:195], v[78:81]
	v_mfma_f32_16x16x32_bf16 v[70:73], v[154:157], v[192:195], v[70:73]
	v_mfma_f32_16x16x32_bf16 v[126:129], v[134:137], v[172:175], v[126:129]
	v_mfma_f32_16x16x32_bf16 v[118:121], v[158:161], v[172:175], v[118:121]
	v_mfma_f32_16x16x32_bf16 v[110:113], v[134:137], v[180:183], v[110:113]
	v_mfma_f32_16x16x32_bf16 v[102:105], v[158:161], v[180:183], v[102:105]
	v_mfma_f32_16x16x32_bf16 v[94:97], v[134:137], v[188:191], v[94:97]
	v_mfma_f32_16x16x32_bf16 v[86:89], v[158:161], v[188:191], v[86:89]
	v_mfma_f32_16x16x32_bf16 v[78:81], v[134:137], v[196:199], v[78:81]
	v_mfma_f32_16x16x32_bf16 v[70:73], v[158:161], v[196:199], v[70:73]
	s_setprio 0
	s_barrier
	s_add_i32 s54, 0, 0x14000
	v_add_u32_e32 v162, s54, v165
	s_add_i32 s0, s49, s65
	ds_read_b128 v[216:219], v162
	ds_read_b128 v[220:223], v162 offset:1024
	ds_read_b128 v[224:227], v162 offset:2048
	ds_read_b128 v[228:231], v162 offset:3072
	v_lshl_add_u64 v[162:163], s[38:39], 0, v[0:1]
	s_mov_b32 m0, s0
	v_lshl_add_u64 v[200:201], s[38:39], 0, v[140:141]
	global_load_lds_dwordx4 v[162:163], off
	s_add_i32 m0, s0, 0x2000
	s_nop 0
	global_load_lds_dwordx4 v[200:201], off
	s_barrier
	s_waitcnt lgkmcnt(0)
	s_setprio 1
	s_waitcnt lgkmcnt(0)
	v_mfma_f32_16x16x32_bf16 v[122:125], v[216:219], v[168:171], v[122:125]
	v_mfma_f32_16x16x32_bf16 v[114:117], v[224:227], v[168:171], v[114:117]
	v_mfma_f32_16x16x32_bf16 v[106:109], v[216:219], v[176:179], v[106:109]
	v_mfma_f32_16x16x32_bf16 v[98:101], v[224:227], v[176:179], v[98:101]
	v_mfma_f32_16x16x32_bf16 v[90:93], v[216:219], v[184:187], v[90:93]
	v_mfma_f32_16x16x32_bf16 v[82:85], v[224:227], v[184:187], v[82:85]
	v_mfma_f32_16x16x32_bf16 v[74:77], v[216:219], v[192:195], v[74:77]
	v_mfma_f32_16x16x32_bf16 v[66:69], v[224:227], v[192:195], v[66:69]
	v_mfma_f32_16x16x32_bf16 v[122:125], v[220:223], v[172:175], v[122:125]
	v_mfma_f32_16x16x32_bf16 v[114:117], v[228:231], v[172:175], v[114:117]
	v_mfma_f32_16x16x32_bf16 v[106:109], v[220:223], v[180:183], v[106:109]
	v_mfma_f32_16x16x32_bf16 v[98:101], v[228:231], v[180:183], v[98:101]
	v_mfma_f32_16x16x32_bf16 v[90:93], v[220:223], v[188:191], v[90:93]
	v_mfma_f32_16x16x32_bf16 v[82:85], v[228:231], v[188:191], v[82:85]
	v_mfma_f32_16x16x32_bf16 v[74:77], v[220:223], v[196:199], v[74:77]
	v_mfma_f32_16x16x32_bf16 v[66:69], v[228:231], v[196:199], v[66:69]
	s_setprio 0
	s_mov_b32 m0, s76
	v_lshl_add_u64 v[232:233], s[42:43], 0, v[142:143]
	s_barrier
	ds_read_b128 v[168:171], v167 offset:16384
	ds_read_b128 v[172:175], v167 offset:17408
	ds_read_b128 v[176:179], v167 offset:18432
	ds_read_b128 v[180:183], v167 offset:19456
	ds_read_b128 v[184:187], v167 offset:20480
	ds_read_b128 v[188:191], v167 offset:21504
	ds_read_b128 v[192:195], v167 offset:22528
	ds_read_b128 v[196:199], v167 offset:23552
	global_load_lds_dwordx4 v[232:233], off
	v_lshl_add_u64 v[234:235], s[42:43], 0, v[146:147]
	s_mov_b32 m0, s77
	s_nop 0
	global_load_lds_dwordx4 v[234:235], off
	s_barrier
	s_waitcnt lgkmcnt(0)
	s_setprio 1
	s_waitcnt lgkmcnt(0)
	v_mfma_f32_16x16x32_bf16 v[62:65], v[130:133], v[168:171], v[62:65]
	v_mfma_f32_16x16x32_bf16 v[54:57], v[154:157], v[168:171], v[54:57]
	v_mfma_f32_16x16x32_bf16 v[46:49], v[130:133], v[176:179], v[46:49]
	v_mfma_f32_16x16x32_bf16 v[38:41], v[154:157], v[176:179], v[38:41]
	v_mfma_f32_16x16x32_bf16 v[30:33], v[130:133], v[184:187], v[30:33]
	v_mfma_f32_16x16x32_bf16 v[22:25], v[154:157], v[184:187], v[22:25]
	v_mfma_f32_16x16x32_bf16 v[10:13], v[130:133], v[192:195], v[10:13]
	v_mfma_f32_16x16x32_bf16 v[2:5], v[154:157], v[192:195], v[2:5]
	v_mfma_f32_16x16x32_bf16 v[62:65], v[134:137], v[172:175], v[62:65]
	v_mfma_f32_16x16x32_bf16 v[54:57], v[158:161], v[172:175], v[54:57]
	v_mfma_f32_16x16x32_bf16 v[46:49], v[134:137], v[180:183], v[46:49]
	v_mfma_f32_16x16x32_bf16 v[38:41], v[158:161], v[180:183], v[38:41]
	v_mfma_f32_16x16x32_bf16 v[30:33], v[134:137], v[188:191], v[30:33]
	v_mfma_f32_16x16x32_bf16 v[22:25], v[158:161], v[188:191], v[22:25]
	v_mfma_f32_16x16x32_bf16 v[10:13], v[134:137], v[196:199], v[10:13]
	v_mfma_f32_16x16x32_bf16 v[2:5], v[158:161], v[196:199], v[2:5]
	s_setprio 0
	s_barrier
; #define G8_STAGE(bufoff, gbase, voff) do { _Pragma("unroll") for (int _i = 0; _i < 2; ++_i) \
;         __builtin_amdgcn_global_load_lds((const unsigned*)((const char*)(gbase) + (voff)[_i]), (LAS unsigned*)(lds + (bufoff) + ldsw + _i * 8192), 16, 0, 0); } while (0)
; #define G8_LDA(dst, b, h) do { _Pragma("unroll") for (int m = 0; m < 4; ++m) _Pragma("unroll") for (int k = 0; k < 2; ++k) dst[m][k] = *(const LAS bf16x8*)(lds + G8_SA(b, h) + aoff + m * 2048 + k * 1024); } while (0)
; #define G8_LDB(dst, b, h) do { _Pragma("unroll") for (int n = 0; n < 2; ++n) _Pragma("unroll") for (int k = 0; k < 2; ++k) dst[n][k] = *(const LAS bf16x8*)(lds + G8_SB(b, h) + boff + n * 2048 + k * 1024); } while (0)
; #define G8_MMA(ai, bj, At, Bt) do { __builtin_amdgcn_s_setprio(1); _Pragma("unroll") for (int m = 0; m < 4; ++m) _Pragma("unroll") for (int n = 0; n < 2; ++n) _Pragma("unroll") for (int k = 0; k < 2; ++k) \
;         acc[ai][bj][m][n] = __builtin_amdgcn_mfma_f32_16x16x32_bf16(Bt[n][k], At[m][k], acc[ai][bj][m][n], 0, 0, 0); __builtin_amdgcn_s_setprio(0); } while (0)
; #define G8_WAIT_V(n) asm volatile("s_waitcnt vmcnt(" #n ")" ::: "memory")
; #define G8_WAIT_L(n) asm volatile("s_waitcnt lgkmcnt(" #n ")" ::: "memory")
; #define G8_BAR __builtin_amdgcn_s_barrier()
; #define G8_SCHED __builtin_amdgcn_sched_barrier(0)
; template <class Epi, class Sched>
; __device__ __forceinline__ void gemm_phase(LAS unsigned char* lds, const int K, const Sched& S, const Epi& E) {
;     ...
;             G8_STAGE(G8_SB(0, 1), b2 + hstep, voffB);
;             G8_WAIT_V(6); G8_BAR; G8_MMA(1, 1, At, B1); G8_BAR;
;             G8_LDB(B0, 1, 0); G8_SCHED; G8_LDA(At, 1, 0); G8_STAGE(G8_SA(0, 1), a2, oc[1]);
;             G8_WAIT_L(8); G8_BAR; G8_WAIT_L(0); G8_MMA(0, 0, At, B0); G8_BAR; G8_SCHED;
;             G8_LDB(B1, 1, 1); G8_STAGE(G8_SB(1, 0), b3, voffB);
;             G8_BAR; G8_WAIT_L(0); G8_MMA(0, 1, At, B1); G8_BAR;
;             G8_LDA(At, 1, 1); G8_STAGE(G8_SA(1, 0), a3, oc[0]);
	s_add_u32 s0, s38, 0x40000
	s_addc_u32 s1, s39, 0
	s_add_i32 s49, s54, s65
	v_lshl_add_u64 v[130:131], s[0:1], 0, v[0:1]
	s_mov_b32 m0, s49
	s_nop 0
	global_load_lds_dwordx4 v[130:131], off
	v_lshl_add_u64 v[130:131], s[0:1], 0, v[140:141]
	s_add_i32 m0, s49, 0x2000
	s_nop 0
	global_load_lds_dwordx4 v[130:131], off
	s_waitcnt vmcnt(6)
	s_barrier
	s_setprio 1
	v_mfma_f32_16x16x32_bf16 v[58:61], v[216:219], v[168:171], v[58:61]
	v_mfma_f32_16x16x32_bf16 v[50:53], v[224:227], v[168:171], v[50:53]
	v_mfma_f32_16x16x32_bf16 v[42:45], v[216:219], v[176:179], v[42:45]
	v_mfma_f32_16x16x32_bf16 v[34:37], v[224:227], v[176:179], v[34:37]
	v_mfma_f32_16x16x32_bf16 v[26:29], v[216:219], v[184:187], v[26:29]
	v_mfma_f32_16x16x32_bf16 v[18:21], v[224:227], v[184:187], v[18:21]
	v_mfma_f32_16x16x32_bf16 v[14:17], v[216:219], v[192:195], v[14:17]
	v_mfma_f32_16x16x32_bf16 v[6:9], v[224:227], v[192:195], v[6:9]
	v_mfma_f32_16x16x32_bf16 v[58:61], v[220:223], v[172:175], v[58:61]
	v_mfma_f32_16x16x32_bf16 v[50:53], v[228:231], v[172:175], v[50:53]
	v_mfma_f32_16x16x32_bf16 v[42:45], v[220:223], v[180:183], v[42:45]
	v_mfma_f32_16x16x32_bf16 v[34:37], v[228:231], v[180:183], v[34:37]
	v_mfma_f32_16x16x32_bf16 v[26:29], v[220:223], v[188:191], v[26:29]
	v_mfma_f32_16x16x32_bf16 v[18:21], v[228:231], v[188:191], v[18:21]
	v_mfma_f32_16x16x32_bf16 v[14:17], v[220:223], v[196:199], v[14:17]
	v_mfma_f32_16x16x32_bf16 v[6:9], v[228:231], v[196:199], v[6:9]
	s_setprio 0
	s_add_i32 s0, 0, 0x18000
	v_add_u32_e32 v158, s0, v165
	s_barrier
	ds_read_b128 v[130:133], v158
	ds_read_b128 v[134:137], v158 offset:1024
	ds_read_b128 v[154:157], v158 offset:2048
	ds_read_b128 v[158:161], v158 offset:3072
	s_mov_b32 m0, s78
	v_lshl_add_u64 v[216:217], s[42:43], 0, v[144:145]
	ds_read_b128 v[168:171], v167 offset:32768
	ds_read_b128 v[172:175], v167 offset:33792
	ds_read_b128 v[176:179], v167 offset:34816
	ds_read_b128 v[180:183], v167 offset:35840
	ds_read_b128 v[184:187], v167 offset:36864
	ds_read_b128 v[188:191], v167 offset:37888
	ds_read_b128 v[192:195], v167 offset:38912
	ds_read_b128 v[196:199], v167 offset:39936
	global_load_lds_dwordx4 v[216:217], off
	v_lshl_add_u64 v[216:217], s[42:43], 0, v[148:149]
	s_mov_b32 m0, s79
	s_nop 0
	global_load_lds_dwordx4 v[216:217], off
	s_waitcnt lgkmcnt(8)
	s_barrier
	s_waitcnt lgkmcnt(0)
	s_setprio 1
	s_waitcnt lgkmcnt(0)
	v_mfma_f32_16x16x32_bf16 v[126:129], v[130:133], v[168:171], v[126:129]
	v_mfma_f32_16x16x32_bf16 v[118:121], v[154:157], v[168:171], v[118:121]
	v_mfma_f32_16x16x32_bf16 v[110:113], v[130:133], v[176:179], v[110:113]
	v_mfma_f32_16x16x32_bf16 v[102:105], v[154:157], v[176:179], v[102:105]
	v_mfma_f32_16x16x32_bf16 v[94:97], v[130:133], v[184:187], v[94:97]
	v_mfma_f32_16x16x32_bf16 v[86:89], v[154:157], v[184:187], v[86:89]
	v_mfma_f32_16x16x32_bf16 v[78:81], v[130:133], v[192:195], v[78:81]
	v_mfma_f32_16x16x32_bf16 v[70:73], v[154:157], v[192:195], v[70:73]
	v_mfma_f32_16x16x32_bf16 v[126:129], v[134:137], v[172:175], v[126:129]
	v_mfma_f32_16x16x32_bf16 v[118:121], v[158:161], v[172:175], v[118:121]
	v_mfma_f32_16x16x32_bf16 v[110:113], v[134:137], v[180:183], v[110:113]
	v_mfma_f32_16x16x32_bf16 v[102:105], v[158:161], v[180:183], v[102:105]
	v_mfma_f32_16x16x32_bf16 v[94:97], v[134:137], v[188:191], v[94:97]
	v_mfma_f32_16x16x32_bf16 v[86:89], v[158:161], v[188:191], v[86:89]
	v_mfma_f32_16x16x32_bf16 v[78:81], v[134:137], v[196:199], v[78:81]
	v_mfma_f32_16x16x32_bf16 v[70:73], v[158:161], v[196:199], v[70:73]
	s_setprio 0
	s_barrier
	s_add_i32 s42, 0, 0x1c000
	s_add_i32 s0, s0, s65
	v_add_u32_e32 v213, s42, v165
	v_lshl_add_u64 v[162:163], v[162:163], 0, s[18:19]
	s_mov_b32 m0, s0
	ds_read_b128 v[216:219], v213
	ds_read_b128 v[220:223], v213 offset:1024
	ds_read_b128 v[224:227], v213 offset:2048
	ds_read_b128 v[228:231], v213 offset:3072
	global_load_lds_dwordx4 v[162:163], off
	v_lshl_add_u64 v[162:163], v[200:201], 0, s[18:19]
	s_add_i32 m0, s0, 0x2000
	s_nop 0
	global_load_lds_dwordx4 v[162:163], off
	s_barrier
	s_waitcnt lgkmcnt(0)
	s_setprio 1
	s_waitcnt lgkmcnt(0)
	v_mfma_f32_16x16x32_bf16 v[122:125], v[216:219], v[168:171], v[122:125]
	v_mfma_f32_16x16x32_bf16 v[114:117], v[224:227], v[168:171], v[114:117]
	v_mfma_f32_16x16x32_bf16 v[106:109], v[216:219], v[176:179], v[106:109]
	v_mfma_f32_16x16x32_bf16 v[98:101], v[224:227], v[176:179], v[98:101]
	v_mfma_f32_16x16x32_bf16 v[90:93], v[216:219], v[184:187], v[90:93]
	v_mfma_f32_16x16x32_bf16 v[82:85], v[224:227], v[184:187], v[82:85]
	v_mfma_f32_16x16x32_bf16 v[74:77], v[216:219], v[192:195], v[74:77]
	v_mfma_f32_16x16x32_bf16 v[66:69], v[224:227], v[192:195], v[66:69]
	v_mfma_f32_16x16x32_bf16 v[122:125], v[220:223], v[172:175], v[122:125]
	v_mfma_f32_16x16x32_bf16 v[114:117], v[228:231], v[172:175], v[114:117]
	v_mfma_f32_16x16x32_bf16 v[106:109], v[220:223], v[180:183], v[106:109]
	v_mfma_f32_16x16x32_bf16 v[98:101], v[228:231], v[180:183], v[98:101]
	v_mfma_f32_16x16x32_bf16 v[90:93], v[220:223], v[188:191], v[90:93]
	v_mfma_f32_16x16x32_bf16 v[82:85], v[228:231], v[188:191], v[82:85]
	v_mfma_f32_16x16x32_bf16 v[74:77], v[220:223], v[196:199], v[74:77]
	v_mfma_f32_16x16x32_bf16 v[66:69], v[228:231], v[196:199], v[66:69]
	s_setprio 0
	s_mov_b32 m0, s81
	v_lshl_add_u64 v[162:163], v[232:233], 0, s[18:19]
	s_barrier
	ds_read_b128 v[168:171], v167 offset:49152
	ds_read_b128 v[172:175], v167 offset:50176
	ds_read_b128 v[176:179], v167 offset:51200
	ds_read_b128 v[180:183], v167 offset:52224
	ds_read_b128 v[184:187], v167 offset:53248
	ds_read_b128 v[188:191], v167 offset:54272
	ds_read_b128 v[192:195], v167 offset:55296
	ds_read_b128 v[196:199], v167 offset:56320
	global_load_lds_dwordx4 v[162:163], off
	v_lshl_add_u64 v[162:163], v[234:235], 0, s[18:19]
	s_mov_b32 m0, s82
	s_nop 0
	global_load_lds_dwordx4 v[162:163], off
	s_barrier
; #define G8_WAIT_V(n) asm volatile("s_waitcnt vmcnt(" #n ")" ::: "memory")
; #define G8_WAIT_L(n) asm volatile("s_waitcnt lgkmcnt(" #n ")" ::: "memory")
; template <class Epi, class Sched>
; __device__ __forceinline__ void gemm_phase(LAS unsigned char* lds, const int K, const Sched& S, const Epi& E) {
;     ...
;             G8_BAR; G8_WAIT_L(0); G8_MMA(1, 0, At, B0); G8_BAR; G8_SCHED;
;             G8_STAGE(G8_SB(1, 1), b3 + hstep, voffB);
;             G8_WAIT_V(6); G8_BAR; G8_MMA(1, 1, At, B1); G8_BAR;
;         }
;     __device__ __forceinline__ void operator()(const f32x4 (&acc)[2][2][4][2], const g8::Unit& u, int wr, int wc, int fr_, int fq_) const {
;     ...
;         const int pn = u.pn; const int colp = pn * 256 + wc * 32 + fq * 8;
;         bf16_t* qb = (bf16_t*)(ws + AB_QB); bf16_t* kb = (bf16_t*)(ws + AB_KB); bf16_t* vT = (bf16_t*)(ws + AB_VT); bf16_t* rqb = (bf16_t*)(ws + AB_RQB); bf16_t* rkb = (bf16_t*)(ws + AB_RKB);
;         bf16_t* rkdT = (bf16_t*)(ws + AB_RKDT); bf16_t* rvT = (bf16_t*)(ws + AB_RVT); bf16_t* rgb = (bf16_t*)(ws + AB_RGB);
;         const float frqA0 = exp2f(-(float)(fq * 8) * (13.287712379549449f / 32.f)) * 0.15915494309189535f;
;         const float frqR0 = exp2f(-(float)((wc & 1) * 32 + fq * 8) * (13.287712379549449f / 63.f)) * 0.15915494309189535f;
;         constexpr float RA[8] = {1.f, 0.7498942093324559f, 0.5623413251903491f, 0.4216965034285822f, 0.31622776601683794f, 0.23713737056616552f, 0.1778279410038923f, 0.1333521432163324f};
;         constexpr float RR[8] = {1.f, 0.8639884494839686f, 0.746476040841712f, 0.6449466771037624f, 0.5572264795507174f, 0.4814372420784346f, 0.4159562163071847f, 0.35938136638046275f};
; #pragma unroll
;         for (int ai = 0; ai < 2; ++ai)
; #pragma unroll
;             for (int m = 0; m < 4; ++m) {
;                 const int t = u.pm * 256 + ai * 128 + wr * 64 + m * 16 + fr, sq = t & (SEQ - 1), b = t >> 13;
;                 f32x4 x[2][2];
; #pragma unroll
;                 for (int bj = 0; bj < 2; ++bj)
; #pragma unroll
;                     for (int n = 0; n < 2; ++n) x[bj][n] = acc[ai][bj][m][n];
;                 if (pn < 4 || (pn == 4 && wc < 2)) {
;                     const int j0 = fq * 8; const float sc = pn < 4 ? 0.125f : 1.f;
;                     u32x4 w1, w2;
; #pragma unroll
;                     for (int n = 0; n < 2; ++n) { f32x4 o1, o2;
; #pragma unroll
	s_waitcnt lgkmcnt(0)
	s_setprio 1
	s_waitcnt lgkmcnt(0)
	v_mfma_f32_16x16x32_bf16 v[62:65], v[130:133], v[168:171], v[62:65]
	v_mfma_f32_16x16x32_bf16 v[54:57], v[154:157], v[168:171], v[54:57]
	v_mfma_f32_16x16x32_bf16 v[46:49], v[130:133], v[176:179], v[46:49]
	v_mfma_f32_16x16x32_bf16 v[38:41], v[154:157], v[176:179], v[38:41]
	v_mfma_f32_16x16x32_bf16 v[30:33], v[130:133], v[184:187], v[30:33]
	v_mfma_f32_16x16x32_bf16 v[22:25], v[154:157], v[184:187], v[22:25]
	v_mfma_f32_16x16x32_bf16 v[10:13], v[130:133], v[192:195], v[10:13]
	v_mfma_f32_16x16x32_bf16 v[2:5], v[154:157], v[192:195], v[2:5]
	v_mfma_f32_16x16x32_bf16 v[62:65], v[134:137], v[172:175], v[62:65]
	v_mfma_f32_16x16x32_bf16 v[54:57], v[158:161], v[172:175], v[54:57]
	v_mfma_f32_16x16x32_bf16 v[46:49], v[134:137], v[180:183], v[46:49]
	v_mfma_f32_16x16x32_bf16 v[38:41], v[158:161], v[180:183], v[38:41]
	v_mfma_f32_16x16x32_bf16 v[30:33], v[134:137], v[188:191], v[30:33]
	v_mfma_f32_16x16x32_bf16 v[22:25], v[158:161], v[188:191], v[22:25]
	v_mfma_f32_16x16x32_bf16 v[10:13], v[134:137], v[196:199], v[10:13]
	v_mfma_f32_16x16x32_bf16 v[2:5], v[158:161], v[196:199], v[2:5]
	s_setprio 0
	s_barrier
	s_add_u32 s0, s38, 0x40080
	s_addc_u32 s1, s39, 0
	s_add_i32 s38, s42, s65
	v_lshl_add_u64 v[130:131], s[0:1], 0, v[0:1]
	s_mov_b32 m0, s38
	s_nop 0
	global_load_lds_dwordx4 v[130:131], off
	v_lshl_add_u64 v[130:131], s[0:1], 0, v[140:141]
	s_add_i32 m0, s38, 0x2000
	s_nop 0
	global_load_lds_dwordx4 v[130:131], off
	s_waitcnt vmcnt(6)
	s_barrier
	s_setprio 1
	v_mfma_f32_16x16x32_bf16 v[58:61], v[216:219], v[168:171], v[58:61]
	v_mfma_f32_16x16x32_bf16 v[50:53], v[224:227], v[168:171], v[50:53]
	v_mfma_f32_16x16x32_bf16 v[42:45], v[216:219], v[176:179], v[42:45]
	v_mfma_f32_16x16x32_bf16 v[34:37], v[224:227], v[176:179], v[34:37]
	v_mfma_f32_16x16x32_bf16 v[26:29], v[216:219], v[184:187], v[26:29]
	v_mfma_f32_16x16x32_bf16 v[18:21], v[224:227], v[184:187], v[18:21]
	v_mfma_f32_16x16x32_bf16 v[14:17], v[216:219], v[192:195], v[14:17]
	v_mfma_f32_16x16x32_bf16 v[6:9], v[224:227], v[192:195], v[6:9]
	v_mfma_f32_16x16x32_bf16 v[58:61], v[220:223], v[172:175], v[58:61]
	v_mfma_f32_16x16x32_bf16 v[50:53], v[228:231], v[172:175], v[50:53]
	v_mfma_f32_16x16x32_bf16 v[42:45], v[220:223], v[180:183], v[42:45]
	v_mfma_f32_16x16x32_bf16 v[34:37], v[228:231], v[180:183], v[34:37]
	v_mfma_f32_16x16x32_bf16 v[26:29], v[220:223], v[188:191], v[26:29]
	v_mfma_f32_16x16x32_bf16 v[18:21], v[228:231], v[188:191], v[18:21]
	v_mfma_f32_16x16x32_bf16 v[14:17], v[220:223], v[196:199], v[14:17]
	v_mfma_f32_16x16x32_bf16 v[6:9], v[228:231], v[196:199], v[6:9]
	s_setprio 0
	s_add_i32 s47, s47, 2
	s_add_u32 s3, s3, 0x100
	s_addc_u32 s14, s14, 0
	s_cmp_gt_u32 s47, 13
	s_mov_b64 s[0:1], s[12:13]
	s_barrier
	s_cbranch_scc0 .LBB0_487
	s_nop 0
	s_nop 0
	s_nop 0
	s_nop 0
	s_nop 0
	s_nop 0
	s_nop 0
	s_nop 0
	s_lshl_b32 s2, s2, 8
	s_add_i32 s2, s2, s80
	s_cmp_lt_i32 s94, 4
	s_cselect_b64 s[36:37], -1, 0
	s_cmp_lg_u32 s94, 4
	v_mov_b32_e32 v131, v164
	v_mov_b32_e32 v130, v139
	s_cselect_b64 s[12:13], -1, 0
	s_cmp_eq_u32 s94, 4
	s_nop 0
	v_add_u32_e32 v160, s2, v131
	s_cselect_b64 s[2:3], -1, 0
	s_and_b64 s[2:3], s[2:3], s[10:11]
	s_cmp_gt_u32 s94, 8
	s_cselect_b64 s[56:57], -1, 0
	s_cmp_gt_u32 s94, 12
	s_cselect_b64 s[54:55], -1, 0
	s_lshl_b32 s42, s94, 8
	s_add_i32 s14, s42, 0xfffff300
	v_lshlrev_b32_e32 v130, 3, v130
	s_lshl_b64 s[22:23], s[14:15], 1
	v_add_u32_e32 v132, s85, v130
	s_add_u32 s22, s87, s22
	v_cvt_f32_i32_e32 v133, v132
	s_addc_u32 s23, s88, s23
	s_add_i32 s14, s86, s42
	s_cmp_gt_u32 s94, 6
	v_add_u32_e32 v171, s14, v130
	s_cselect_b64 s[38:39], -1, 0
	s_lshl_b32 s14, s94, 1
	s_and_b32 s14, s14, 2
	v_mul_f32_e32 v134, 0xbe57fa62, v133
	s_or_b32 s14, s14, s89
	v_cmp_gt_f32_e32 vcc, s66, v134
	v_ashrrev_i32_e32 v131, 31, v130
	s_lshl_b32 s14, s14, 7
	v_cvt_f32_i32_e32 v172, v130
	v_cndmask_b32_e32 v134, 0, v207, vcc
	v_lshlrev_b64 v[162:163], 1, v[130:131]
	s_xor_b32 s14, s14, 0x100
	v_fmac_f32_e32 v134, 0xbe57fa62, v133
	v_lshl_add_u64 v[158:159], s[22:23], 0, v[162:163]
	s_and_b64 s[22:23], s[38:39], exec
	v_exp_f32_e32 v133, v134
	s_mov_b32 s22, 0x3d420000
	s_cselect_b32 s22, s22, 0x3c420000
	v_mul_f32_e32 v134, 0xbed49a78, v172
	s_add_u32 s22, s40, s22
	v_cmp_gt_f32_e64 s[0:1], s66, v134
	v_cndmask_b32_e32 v134, 0, v208, vcc
	v_add_u32_e32 v170, s14, v132
	s_addc_u32 s23, s41, 0
	s_lshl_b32 s14, s14, 1
	v_ldexp_f32 v133, v133, v134
	s_add_u32 s22, s22, s14
	v_mul_f32_e32 v169, 0.15915494, v133
	s_addc_u32 s23, s23, 0
	v_ashrrev_i32_e32 v133, 31, v132
	v_lshl_add_u64 v[154:155], v[132:133], 1, s[22:23]
	s_or_b32 s22, s42, s75
	s_ashr_i32 s23, s22, 31
	s_lshl_b64 s[22:23], s[22:23], 1
	s_add_u32 s42, s83, s22
	v_mov_b32_e32 v131, 0x3db504f3
	s_addc_u32 s43, s84, s23
	s_nor_b64 s[22:23], s[36:37], s[2:3]
	v_cndmask_b32_e64 v156, 1.0, v131, s[38:39]
	v_add_u32_e32 v168, s90, v130
	v_and_b32_e32 v173, 0x1fff, v160
	s_mov_b64 s[2:3], -1
	s_and_b64 vcc, exec, s[22:23]
	s_cbranch_vccz .LBB0_506
; __device__ __forceinline__ unsigned pk2(float lo, float hi) { unsigned r; asm("v_cvt_pk_bf16_f32 %0, %1, %2" : "=v"(r) : "v"(lo), "v"(hi)); return r; }
; __device__ __forceinline__ f32x4 silu4(const f32x4 x) { const f32x4 t = x * (-1.4426950408889634f); f32x4 d;
; #pragma unroll
;     for (int e = 0; e < 4; ++e) d[e] = __builtin_amdgcn_exp2f(t[e]);
;     d = d + 1.f;
; #pragma unroll
;     for (int e = 0; e < 4; ++e) d[e] = __builtin_amdgcn_rcpf(d[e]);
;     return x * d; }
;     __device__ __forceinline__ void operator()(const f32x4 (&acc)[2][2][4][2], const g8::Unit& u, int wr, int wc, int fr_, int fq_) const {
;     ...
;                 } else {
; #pragma unroll
;                     for (int bj = 0; bj < 2; ++bj) { u32x4 w;
; #pragma unroll
;                         for (int n = 0; n < 2; ++n) { const f32x4 sv = silu4(x[bj][n]); w[2 * n] = pk2(sv[0], sv[1]); w[2 * n + 1] = pk2(sv[2], sv[3]); }
;                         *(u32x4*)(rgb + (size_t)t * 1024 + (pn - 13) * 256 + bj * 128 + wc * 32 + fq * 8) = w; }
	v_ashrrev_i32_e32 v174, 13, v160
	s_and_b64 vcc, exec, s[12:13]
	s_cbranch_vccz .LBB0_503
	s_and_b64 vcc, exec, s[56:57]
	s_cbranch_vccz .LBB0_496
	s_andn2_b64 vcc, exec, s[54:55]
	s_cbranch_vccnz .LBB0_493
	v_mul_f32_e32 v132, 0xbfb8aa3b, v126
	v_mul_f32_e32 v133, 0xbfb8aa3b, v127
	v_mul_f32_e32 v134, 0xbfb8aa3b, v128
	v_mul_f32_e32 v135, 0xbfb8aa3b, v129
	v_exp_f32_e32 v132, v132
	v_exp_f32_e32 v133, v133
	v_exp_f32_e32 v134, v134
	v_exp_f32_e32 v135, v135
	v_mul_f32_e32 v136, 0xbfb8aa3b, v120
	v_pk_add_f32 v[132:133], v[132:133], 1.0 op_sel_hi:[1,0]
	v_mul_f32_e32 v137, 0xbfb8aa3b, v121
	v_pk_add_f32 v[134:135], v[134:135], 1.0 op_sel_hi:[1,0]
	v_rcp_f32_e32 v132, v132
	v_rcp_f32_e32 v133, v133
	v_rcp_f32_e32 v134, v134
	v_rcp_f32_e32 v135, v135
	v_exp_f32_e32 v136, v136
	v_pk_mul_f32 v[132:133], v[126:127], v[132:133]
	v_exp_f32_e32 v137, v137
	v_pk_mul_f32 v[134:135], v[128:129], v[134:135]
	v_cvt_pk_bf16_f32 v132, v132, v133
	v_ashrrev_i32_e32 v161, 31, v160
	v_cvt_pk_bf16_f32 v133, v134, v135
	v_mul_f32_e32 v134, 0xbfb8aa3b, v118
	v_mul_f32_e32 v135, 0xbfb8aa3b, v119
	v_exp_f32_e32 v134, v134
	v_exp_f32_e32 v135, v135
	v_pk_add_f32 v[136:137], v[136:137], 1.0 op_sel_hi:[1,0]
	v_lshlrev_b64 v[130:131], 11, v[160:161]
	v_rcp_f32_e32 v136, v136
	v_pk_add_f32 v[134:135], v[134:135], 1.0 op_sel_hi:[1,0]
	v_rcp_f32_e32 v137, v137
	v_rcp_f32_e32 v134, v134
	v_rcp_f32_e32 v135, v135
	v_lshl_add_u64 v[130:131], v[158:159], 0, v[130:131]
	v_pk_mul_f32 v[136:137], v[120:121], v[136:137]
	s_mov_b64 s[2:3], 0
	v_pk_mul_f32 v[134:135], v[118:119], v[134:135]
	s_nop 0
	v_cvt_pk_bf16_f32 v134, v134, v135
	v_cvt_pk_bf16_f32 v135, v136, v137
	global_store_dwordx4 v[130:131], v[132:135], off
	v_mul_f32_e32 v136, 0xbfb8aa3b, v116
	v_mul_f32_e32 v137, 0xbfb8aa3b, v117
	v_mul_f32_e32 v132, 0xbfb8aa3b, v122
	v_mul_f32_e32 v133, 0xbfb8aa3b, v123
	v_mul_f32_e32 v134, 0xbfb8aa3b, v124
	v_mul_f32_e32 v135, 0xbfb8aa3b, v125
	v_exp_f32_e32 v132, v132
	v_exp_f32_e32 v133, v133
	v_exp_f32_e32 v134, v134
	v_exp_f32_e32 v135, v135
	v_exp_f32_e32 v136, v136
	v_pk_add_f32 v[132:133], v[132:133], 1.0 op_sel_hi:[1,0]
	v_exp_f32_e32 v137, v137
	v_pk_add_f32 v[134:135], v[134:135], 1.0 op_sel_hi:[1,0]
	v_rcp_f32_e32 v132, v132
	v_rcp_f32_e32 v133, v133
	v_rcp_f32_e32 v134, v134
	v_rcp_f32_e32 v135, v135
	v_pk_add_f32 v[136:137], v[136:137], 1.0 op_sel_hi:[1,0]
	v_pk_mul_f32 v[132:133], v[122:123], v[132:133]
	v_rcp_f32_e32 v136, v136
	v_pk_mul_f32 v[134:135], v[124:125], v[134:135]
	v_cvt_pk_bf16_f32 v132, v132, v133
	v_rcp_f32_e32 v137, v137
	v_cvt_pk_bf16_f32 v133, v134, v135
	v_mul_f32_e32 v134, 0xbfb8aa3b, v114
	v_mul_f32_e32 v135, 0xbfb8aa3b, v115
	v_exp_f32_e32 v134, v134
	v_exp_f32_e32 v135, v135
	v_pk_mul_f32 v[136:137], v[116:117], v[136:137]
	v_pk_add_f32 v[134:135], v[134:135], 1.0 op_sel_hi:[1,0]
	s_nop 0
	v_rcp_f32_e32 v134, v134
	v_rcp_f32_e32 v135, v135
	s_nop 0
	v_pk_mul_f32 v[134:135], v[114:115], v[134:135]
	s_nop 0
	v_cvt_pk_bf16_f32 v134, v134, v135
	v_cvt_pk_bf16_f32 v135, v136, v137
	global_store_dwordx4 v[130:131], v[132:135], off offset:256

; #define G8_STAGE(bufoff, gbase, voff) do { _Pragma("unroll") for (int _i = 0; _i < 2; ++_i) \
;         __builtin_amdgcn_global_load_lds((const unsigned*)((const char*)(gbase) + (voff)[_i]), (LAS unsigned*)(lds + (bufoff) + ldsw + _i * 8192), 16, 0, 0); } while (0)
; #define G8_LDA(dst, b, h) do { _Pragma("unroll") for (int m = 0; m < 4; ++m) _Pragma("unroll") for (int k = 0; k < 2; ++k) dst[m][k] = *(const LAS bf16x8*)(lds + G8_SA(b, h) + aoff + m * 2048 + k * 1024); } while (0)
; #define G8_LDB(dst, b, h) do { _Pragma("unroll") for (int n = 0; n < 2; ++n) _Pragma("unroll") for (int k = 0; k < 2; ++k) dst[n][k] = *(const LAS bf16x8*)(lds + G8_SB(b, h) + boff + n * 2048 + k * 1024); } while (0)
; #define G8_WAIT_L(n) asm volatile("s_waitcnt lgkmcnt(" #n ")" ::: "memory")
; #define G8_BAR __builtin_amdgcn_s_barrier()
;     __device__ __forceinline__ void init(f32x4 (&acc)[2][2][4][2], const Unit& u, int wc, int fq) const {
;         const int col0 = u.pn * BM + wc * 32 + 8 * fq;
; #pragma unroll
;         for (int b = 0; b < 2; ++b)
; #pragma unroll
;             for (int n = 0; n < 2; ++n) { const f32x4 bv = *(const f32x4*)(bias + col0 + b * HALF + 4 * n);
; #pragma unroll
;                 for (int a = 0; a < 2; ++a)
; #pragma unroll
;                     for (int m = 0; m < 4; ++m) acc[a][b][m][n] = bv; } }
; template <class Epi, class Sched>
; __device__ __forceinline__ void gemm_phase(LAS unsigned char* lds, const int K, const Sched& S, const Epi& E) {
;     ...
;         const bool has_next = S.next(ui + 1, nxt);
;         const char* nA = has_next ? nxt.A : cA; const char* nB = has_next ? nxt.B : cB;
; #pragma unroll 1
;         for (int t = 0; t < nt; t += 2) {
;             const bool last = (t == nt - 2);
;             const char* a1 = cA + (size_t)(t + 1) * kstep;
;             const char* a2 = last ? nA : cA + (size_t)(t + 2) * kstep; const char* b2 = last ? nB : cB + (size_t)(t + 2) * kstep;
;             const char* a3 = a2 + kstep; const char* b3 = b2 + kstep;
;             G8_LDB(B0, 0, 0); G8_SCHED; G8_LDA(At, 0, 0); G8_STAGE(G8_SA(1, 1), a1, oc[1]);
;             if (last && has_next) S.aoff(nxt, tid, oc);
;             G8_WAIT_L(8); G8_BAR; G8_WAIT_L(0); G8_MMA(0, 0, At, B0); G8_BAR; G8_SCHED;
;             G8_LDB(B1, 0, 1); G8_STAGE(G8_SB(0, 0), b2, voffB);
;             G8_BAR; G8_WAIT_L(0); G8_MMA(0, 1, At, B1); G8_BAR;
.LBB0_2251:
	s_add_u32 s12, s12, 0x80
	v_mov_b64_e32 v[18:19], 0x100
	s_addc_u32 s13, s13, 0
	v_cmp_lt_i64_e32 vcc, s[24:25], v[18:19]
	s_add_u32 s58, s22, 0x100
	s_waitcnt vmcnt(0)
	v_mov_b64_e32 v[20:21], v[4:5]
	v_mov_b64_e32 v[24:25], v[8:9]
	v_mov_b64_e32 v[36:37], v[4:5]
	v_mov_b64_e32 v[40:41], v[8:9]
	v_mov_b64_e32 v[52:53], v[4:5]
	v_mov_b64_e32 v[56:57], v[8:9]
	v_mov_b64_e32 v[28:29], v[12:13]
	v_mov_b64_e32 v[32:33], v[16:17]
	v_mov_b64_e32 v[44:45], v[12:13]
	v_mov_b64_e32 v[48:49], v[16:17]
	v_mov_b64_e32 v[60:61], v[12:13]
	v_mov_b64_e32 v[64:65], v[16:17]
	v_mov_b64_e32 v[68:69], v[4:5]
	v_mov_b64_e32 v[72:73], v[8:9]
	v_mov_b64_e32 v[84:85], v[4:5]
	v_mov_b64_e32 v[88:89], v[8:9]
	v_mov_b64_e32 v[100:101], v[4:5]
	v_mov_b64_e32 v[104:105], v[8:9]
	v_mov_b64_e32 v[116:117], v[4:5]
	v_mov_b64_e32 v[120:121], v[8:9]
	v_mov_b64_e32 v[76:77], v[12:13]
	v_mov_b64_e32 v[80:81], v[16:17]
	v_mov_b64_e32 v[92:93], v[12:13]
	v_mov_b64_e32 v[96:97], v[16:17]
	v_mov_b64_e32 v[108:109], v[12:13]
	v_mov_b64_e32 v[112:113], v[16:17]
	v_mov_b64_e32 v[124:125], v[12:13]
	v_mov_b64_e32 v[128:129], v[16:17]
	s_addc_u32 s59, s23, 0
	s_mov_b32 s22, 0
	v_mov_b64_e32 v[18:19], v[2:3]
	v_mov_b64_e32 v[22:23], v[6:7]
	v_mov_b64_e32 v[34:35], v[2:3]
	v_mov_b64_e32 v[38:39], v[6:7]
	v_mov_b64_e32 v[50:51], v[2:3]
	v_mov_b64_e32 v[54:55], v[6:7]
	v_mov_b64_e32 v[26:27], v[10:11]
	v_mov_b64_e32 v[30:31], v[14:15]
	v_mov_b64_e32 v[42:43], v[10:11]
	v_mov_b64_e32 v[46:47], v[14:15]
	v_mov_b64_e32 v[58:59], v[10:11]
	v_mov_b64_e32 v[62:63], v[14:15]
	v_mov_b64_e32 v[66:67], v[2:3]
	v_mov_b64_e32 v[70:71], v[6:7]
	v_mov_b64_e32 v[82:83], v[2:3]
	v_mov_b64_e32 v[86:87], v[6:7]
	v_mov_b64_e32 v[98:99], v[2:3]
	v_mov_b64_e32 v[102:103], v[6:7]
	v_mov_b64_e32 v[114:115], v[2:3]
	v_mov_b64_e32 v[118:119], v[6:7]
	v_mov_b64_e32 v[74:75], v[10:11]
	v_mov_b64_e32 v[78:79], v[14:15]
	v_mov_b64_e32 v[90:91], v[10:11]
	v_mov_b64_e32 v[94:95], v[14:15]
	v_mov_b64_e32 v[106:107], v[10:11]
	v_mov_b64_e32 v[110:111], v[14:15]
	v_mov_b64_e32 v[122:123], v[10:11]
	v_mov_b64_e32 v[126:127], v[14:15]
	s_nop 0
	s_nop 0
	s_nop 0
	s_nop 0
	s_nop 0
	s_nop 0
	s_nop 0
	s_nop 0
	s_nop 0
.LBB0_2252:
	s_add_i32 s60, s22, 2
	s_add_u32 s24, s12, 0x80
	s_addc_u32 s23, s13, 0
	s_add_i32 s61, 0, 0x10000
	v_add_u32_e32 v144, s61, v148
	ds_read_b128 v[152:155], v144
	ds_read_b128 v[156:159], v144 offset:1024
	ds_read_b128 v[160:163], v144 offset:2048
	ds_read_b128 v[164:167], v144 offset:3072
	s_cmp_eq_u32 s51, s22
	s_cselect_b32 s22, s0, s24
	s_cselect_b32 s23, s1, s23
	s_cselect_b32 s25, s11, s59
	s_cselect_b32 s24, s10, s58
	v_lshl_add_u64 v[144:145], s[12:13], 0, v[140:141]
	s_add_i32 m0, s44, 0xc000
	ds_read_b128 v[168:171], v150
	ds_read_b128 v[172:175], v150 offset:1024
	ds_read_b128 v[176:179], v150 offset:2048
	ds_read_b128 v[180:183], v150 offset:3072
	ds_read_b128 v[184:187], v150 offset:4096
	ds_read_b128 v[188:191], v150 offset:5120
	ds_read_b128 v[192:195], v150 offset:6144
	ds_read_b128 v[196:199], v150 offset:7168
	global_load_lds_dwordx4 v[144:145], off
	v_lshl_add_u64 v[144:145], s[12:13], 0, v[142:143]
	s_add_i32 m0, s44, 0xe000
	s_nop 0
	global_load_lds_dwordx4 v[144:145], off
	s_waitcnt lgkmcnt(8)
	s_barrier
	s_waitcnt lgkmcnt(0)
	s_setprio 1
	s_waitcnt lgkmcnt(0)
	v_mfma_f32_16x16x32_bf16 v[126:129], v[152:155], v[168:171], v[126:129]
	v_mfma_f32_16x16x32_bf16 v[122:125], v[160:163], v[168:171], v[122:125]
	v_mfma_f32_16x16x32_bf16 v[110:113], v[152:155], v[176:179], v[110:113]
	v_mfma_f32_16x16x32_bf16 v[106:109], v[160:163], v[176:179], v[106:109]
	v_mfma_f32_16x16x32_bf16 v[94:97], v[152:155], v[184:187], v[94:97]
	v_mfma_f32_16x16x32_bf16 v[90:93], v[160:163], v[184:187], v[90:93]
	v_mfma_f32_16x16x32_bf16 v[78:81], v[152:155], v[192:195], v[78:81]
	v_mfma_f32_16x16x32_bf16 v[74:77], v[160:163], v[192:195], v[74:77]
	v_mfma_f32_16x16x32_bf16 v[126:129], v[156:159], v[172:175], v[126:129]
	v_mfma_f32_16x16x32_bf16 v[122:125], v[164:167], v[172:175], v[122:125]
	v_mfma_f32_16x16x32_bf16 v[110:113], v[156:159], v[180:183], v[110:113]
	v_mfma_f32_16x16x32_bf16 v[106:109], v[164:167], v[180:183], v[106:109]
	v_mfma_f32_16x16x32_bf16 v[94:97], v[156:159], v[188:191], v[94:97]
	v_mfma_f32_16x16x32_bf16 v[90:93], v[164:167], v[188:191], v[90:93]
	v_mfma_f32_16x16x32_bf16 v[78:81], v[156:159], v[196:199], v[78:81]
	v_mfma_f32_16x16x32_bf16 v[74:77], v[164:167], v[196:199], v[74:77]
	s_setprio 0
	s_barrier
	s_add_i32 s62, 0, 0x14000
	v_add_u32_e32 v144, s62, v148
	s_add_i32 s61, s61, s43
	ds_read_b128 v[216:219], v144
	ds_read_b128 v[220:223], v144 offset:1024
	ds_read_b128 v[224:227], v144 offset:2048
	ds_read_b128 v[228:231], v144 offset:3072
	v_lshl_add_u64 v[144:145], s[24:25], 0, v[0:1]
	s_mov_b32 m0, s61
	v_lshl_add_u64 v[200:201], s[24:25], 0, v[130:131]
	global_load_lds_dwordx4 v[144:145], off
	s_add_i32 m0, s61, 0x2000
	s_nop 0
	global_load_lds_dwordx4 v[200:201], off
	s_barrier
	s_waitcnt lgkmcnt(0)
	s_setprio 1
	s_waitcnt lgkmcnt(0)
	v_mfma_f32_16x16x32_bf16 v[118:121], v[216:219], v[168:171], v[118:121]
	v_mfma_f32_16x16x32_bf16 v[114:117], v[224:227], v[168:171], v[114:117]
	v_mfma_f32_16x16x32_bf16 v[102:105], v[216:219], v[176:179], v[102:105]
	v_mfma_f32_16x16x32_bf16 v[98:101], v[224:227], v[176:179], v[98:101]
	v_mfma_f32_16x16x32_bf16 v[86:89], v[216:219], v[184:187], v[86:89]
	v_mfma_f32_16x16x32_bf16 v[82:85], v[224:227], v[184:187], v[82:85]
	v_mfma_f32_16x16x32_bf16 v[70:73], v[216:219], v[192:195], v[70:73]
	v_mfma_f32_16x16x32_bf16 v[66:69], v[224:227], v[192:195], v[66:69]
	v_mfma_f32_16x16x32_bf16 v[118:121], v[220:223], v[172:175], v[118:121]
	v_mfma_f32_16x16x32_bf16 v[114:117], v[228:231], v[172:175], v[114:117]
	v_mfma_f32_16x16x32_bf16 v[102:105], v[220:223], v[180:183], v[102:105]
	v_mfma_f32_16x16x32_bf16 v[98:101], v[228:231], v[180:183], v[98:101]
	v_mfma_f32_16x16x32_bf16 v[86:89], v[220:223], v[188:191], v[86:89]
	v_mfma_f32_16x16x32_bf16 v[82:85], v[228:231], v[188:191], v[82:85]
	v_mfma_f32_16x16x32_bf16 v[70:73], v[220:223], v[196:199], v[70:73]
	v_mfma_f32_16x16x32_bf16 v[66:69], v[228:231], v[196:199], v[66:69]
	s_setprio 0
	s_mov_b32 m0, s44
	v_lshl_add_u64 v[232:233], s[22:23], 0, v[132:133]
	s_barrier
; #define G8_STAGE(bufoff, gbase, voff) do { _Pragma("unroll") for (int _i = 0; _i < 2; ++_i) \
;         __builtin_amdgcn_global_load_lds((const unsigned*)((const char*)(gbase) + (voff)[_i]), (LAS unsigned*)(lds + (bufoff) + ldsw + _i * 8192), 16, 0, 0); } while (0)
; #define G8_LDA(dst, b, h) do { _Pragma("unroll") for (int m = 0; m < 4; ++m) _Pragma("unroll") for (int k = 0; k < 2; ++k) dst[m][k] = *(const LAS bf16x8*)(lds + G8_SA(b, h) + aoff + m * 2048 + k * 1024); } while (0)
; #define G8_LDB(dst, b, h) do { _Pragma("unroll") for (int n = 0; n < 2; ++n) _Pragma("unroll") for (int k = 0; k < 2; ++k) dst[n][k] = *(const LAS bf16x8*)(lds + G8_SB(b, h) + boff + n * 2048 + k * 1024); } while (0)
; #define G8_MMA(ai, bj, At, Bt) do { __builtin_amdgcn_s_setprio(1); _Pragma("unroll") for (int m = 0; m < 4; ++m) _Pragma("unroll") for (int n = 0; n < 2; ++n) _Pragma("unroll") for (int k = 0; k < 2; ++k) \
;         acc[ai][bj][m][n] = __builtin_amdgcn_mfma_f32_16x16x32_bf16(Bt[n][k], At[m][k], acc[ai][bj][m][n], 0, 0, 0); __builtin_amdgcn_s_setprio(0); } while (0)
; #define G8_WAIT_V(n) asm volatile("s_waitcnt vmcnt(" #n ")" ::: "memory")
; #define G8_WAIT_L(n) asm volatile("s_waitcnt lgkmcnt(" #n ")" ::: "memory")
; #define G8_BAR __builtin_amdgcn_s_barrier()
; #define G8_SCHED __builtin_amdgcn_sched_barrier(0)
; template <class Epi, class Sched>
; __device__ __forceinline__ void gemm_phase(LAS unsigned char* lds, const int K, const Sched& S, const Epi& E) {
;     ...
;             G8_LDA(At, 0, 1); G8_STAGE(G8_SA(0, 0), a2, oc[0]);
;             G8_BAR; G8_WAIT_L(0); G8_MMA(1, 0, At, B0); G8_BAR; G8_SCHED;
;             G8_STAGE(G8_SB(0, 1), b2 + hstep, voffB);
;             G8_WAIT_V(6); G8_BAR; G8_MMA(1, 1, At, B1); G8_BAR;
;             G8_LDB(B0, 1, 0); G8_SCHED; G8_LDA(At, 1, 0); G8_STAGE(G8_SA(0, 1), a2, oc[1]);
;             G8_WAIT_L(8); G8_BAR; G8_WAIT_L(0); G8_MMA(0, 0, At, B0); G8_BAR; G8_SCHED;
;             G8_LDB(B1, 1, 1); G8_STAGE(G8_SB(1, 0), b3, voffB);
	ds_read_b128 v[168:171], v150 offset:16384
	ds_read_b128 v[172:175], v150 offset:17408
	ds_read_b128 v[176:179], v150 offset:18432
	ds_read_b128 v[180:183], v150 offset:19456
	ds_read_b128 v[184:187], v150 offset:20480
	ds_read_b128 v[188:191], v150 offset:21504
	ds_read_b128 v[192:195], v150 offset:22528
	ds_read_b128 v[196:199], v150 offset:23552
	global_load_lds_dwordx4 v[232:233], off
	v_lshl_add_u64 v[234:235], s[22:23], 0, v[136:137]
	s_mov_b32 m0, s45
	s_nop 0
	global_load_lds_dwordx4 v[234:235], off
	s_barrier
	s_waitcnt lgkmcnt(0)
	s_setprio 1
	s_waitcnt lgkmcnt(0)
	v_mfma_f32_16x16x32_bf16 v[62:65], v[152:155], v[168:171], v[62:65]
	v_mfma_f32_16x16x32_bf16 v[58:61], v[160:163], v[168:171], v[58:61]
	v_mfma_f32_16x16x32_bf16 v[46:49], v[152:155], v[176:179], v[46:49]
	v_mfma_f32_16x16x32_bf16 v[42:45], v[160:163], v[176:179], v[42:45]
	v_mfma_f32_16x16x32_bf16 v[30:33], v[152:155], v[184:187], v[30:33]
	v_mfma_f32_16x16x32_bf16 v[26:29], v[160:163], v[184:187], v[26:29]
	v_mfma_f32_16x16x32_bf16 v[14:17], v[152:155], v[192:195], v[14:17]
	v_mfma_f32_16x16x32_bf16 v[10:13], v[160:163], v[192:195], v[10:13]
	v_mfma_f32_16x16x32_bf16 v[62:65], v[156:159], v[172:175], v[62:65]
	v_mfma_f32_16x16x32_bf16 v[58:61], v[164:167], v[172:175], v[58:61]
	v_mfma_f32_16x16x32_bf16 v[46:49], v[156:159], v[180:183], v[46:49]
	v_mfma_f32_16x16x32_bf16 v[42:45], v[164:167], v[180:183], v[42:45]
	v_mfma_f32_16x16x32_bf16 v[30:33], v[156:159], v[188:191], v[30:33]
	v_mfma_f32_16x16x32_bf16 v[26:29], v[164:167], v[188:191], v[26:29]
	v_mfma_f32_16x16x32_bf16 v[14:17], v[156:159], v[196:199], v[14:17]
	v_mfma_f32_16x16x32_bf16 v[10:13], v[164:167], v[196:199], v[10:13]
	s_setprio 0
	s_barrier
	s_add_u32 s24, s24, s42
	s_addc_u32 s25, s25, 0
	s_add_i32 s61, s62, s43
	v_lshl_add_u64 v[236:237], s[24:25], 0, v[0:1]
	s_mov_b32 m0, s61
	v_lshl_add_u64 v[238:239], s[24:25], 0, v[130:131]
	global_load_lds_dwordx4 v[236:237], off
	s_add_i32 m0, s61, 0x2000
	s_nop 0
	global_load_lds_dwordx4 v[238:239], off
	s_waitcnt vmcnt(6)
	s_barrier
	s_setprio 1
	v_mfma_f32_16x16x32_bf16 v[54:57], v[216:219], v[168:171], v[54:57]
	v_mfma_f32_16x16x32_bf16 v[50:53], v[224:227], v[168:171], v[50:53]
	v_mfma_f32_16x16x32_bf16 v[38:41], v[216:219], v[176:179], v[38:41]
	v_mfma_f32_16x16x32_bf16 v[34:37], v[224:227], v[176:179], v[34:37]
	v_mfma_f32_16x16x32_bf16 v[22:25], v[216:219], v[184:187], v[22:25]
	v_mfma_f32_16x16x32_bf16 v[18:21], v[224:227], v[184:187], v[18:21]
	v_mfma_f32_16x16x32_bf16 v[6:9], v[216:219], v[192:195], v[6:9]
	v_mfma_f32_16x16x32_bf16 v[2:5], v[224:227], v[192:195], v[2:5]
	v_mfma_f32_16x16x32_bf16 v[54:57], v[220:223], v[172:175], v[54:57]
	v_mfma_f32_16x16x32_bf16 v[50:53], v[228:231], v[172:175], v[50:53]
	v_mfma_f32_16x16x32_bf16 v[38:41], v[220:223], v[180:183], v[38:41]
	v_mfma_f32_16x16x32_bf16 v[34:37], v[228:231], v[180:183], v[34:37]
	v_mfma_f32_16x16x32_bf16 v[22:25], v[220:223], v[188:191], v[22:25]
	v_mfma_f32_16x16x32_bf16 v[18:21], v[228:231], v[188:191], v[18:21]
	v_mfma_f32_16x16x32_bf16 v[6:9], v[220:223], v[196:199], v[6:9]
	v_mfma_f32_16x16x32_bf16 v[2:5], v[228:231], v[196:199], v[2:5]
	s_setprio 0
	s_add_i32 s24, 0, 0x18000
	v_add_u32_e32 v151, s24, v148
	s_barrier
	ds_read_b128 v[152:155], v151
	ds_read_b128 v[156:159], v151 offset:1024
	ds_read_b128 v[160:163], v151 offset:2048
	ds_read_b128 v[164:167], v151 offset:3072
	s_mov_b32 m0, s46
	v_lshl_add_u64 v[216:217], s[22:23], 0, v[134:135]
	ds_read_b128 v[168:171], v150 offset:32768
	ds_read_b128 v[172:175], v150 offset:33792
	ds_read_b128 v[176:179], v150 offset:34816
	ds_read_b128 v[180:183], v150 offset:35840
	ds_read_b128 v[184:187], v150 offset:36864
	ds_read_b128 v[188:191], v150 offset:37888
	ds_read_b128 v[192:195], v150 offset:38912
	ds_read_b128 v[196:199], v150 offset:39936
	global_load_lds_dwordx4 v[216:217], off
	v_lshl_add_u64 v[216:217], s[22:23], 0, v[138:139]
	s_mov_b32 m0, s47
	s_nop 0
	global_load_lds_dwordx4 v[216:217], off
	s_waitcnt lgkmcnt(8)
	s_barrier
	s_waitcnt lgkmcnt(0)
	s_setprio 1
	s_waitcnt lgkmcnt(0)
	v_mfma_f32_16x16x32_bf16 v[126:129], v[152:155], v[168:171], v[126:129]
	v_mfma_f32_16x16x32_bf16 v[122:125], v[160:163], v[168:171], v[122:125]
	v_mfma_f32_16x16x32_bf16 v[110:113], v[152:155], v[176:179], v[110:113]
	v_mfma_f32_16x16x32_bf16 v[106:109], v[160:163], v[176:179], v[106:109]
	v_mfma_f32_16x16x32_bf16 v[94:97], v[152:155], v[184:187], v[94:97]
	v_mfma_f32_16x16x32_bf16 v[90:93], v[160:163], v[184:187], v[90:93]
	v_mfma_f32_16x16x32_bf16 v[78:81], v[152:155], v[192:195], v[78:81]
	v_mfma_f32_16x16x32_bf16 v[74:77], v[160:163], v[192:195], v[74:77]
	v_mfma_f32_16x16x32_bf16 v[126:129], v[156:159], v[172:175], v[126:129]
	v_mfma_f32_16x16x32_bf16 v[122:125], v[164:167], v[172:175], v[122:125]
	v_mfma_f32_16x16x32_bf16 v[110:113], v[156:159], v[180:183], v[110:113]
	v_mfma_f32_16x16x32_bf16 v[106:109], v[164:167], v[180:183], v[106:109]
	v_mfma_f32_16x16x32_bf16 v[94:97], v[156:159], v[188:191], v[94:97]
	v_mfma_f32_16x16x32_bf16 v[90:93], v[164:167], v[188:191], v[90:93]
	v_mfma_f32_16x16x32_bf16 v[78:81], v[156:159], v[196:199], v[78:81]
	v_mfma_f32_16x16x32_bf16 v[74:77], v[164:167], v[196:199], v[74:77]
	s_setprio 0
	s_barrier
	s_add_i32 s22, 0, 0x1c000
	s_add_i32 s23, s24, s43
	v_add_u32_e32 v151, s22, v148
	v_lshl_add_u64 v[144:145], v[144:145], 0, s[18:19]
	s_mov_b32 m0, s23
	ds_read_b128 v[216:219], v151
	ds_read_b128 v[220:223], v151 offset:1024
	ds_read_b128 v[224:227], v151 offset:2048
	ds_read_b128 v[228:231], v151 offset:3072
	global_load_lds_dwordx4 v[144:145], off
	v_lshl_add_u64 v[144:145], v[200:201], 0, s[18:19]
	s_add_i32 m0, s23, 0x2000
	s_nop 0
	global_load_lds_dwordx4 v[144:145], off
	s_barrier
; #define G8_STAGE(bufoff, gbase, voff) do { _Pragma("unroll") for (int _i = 0; _i < 2; ++_i) \
;         __builtin_amdgcn_global_load_lds((const unsigned*)((const char*)(gbase) + (voff)[_i]), (LAS unsigned*)(lds + (bufoff) + ldsw + _i * 8192), 16, 0, 0); } while (0)
; #define G8_LDA(dst, b, h) do { _Pragma("unroll") for (int m = 0; m < 4; ++m) _Pragma("unroll") for (int k = 0; k < 2; ++k) dst[m][k] = *(const LAS bf16x8*)(lds + G8_SA(b, h) + aoff + m * 2048 + k * 1024); } while (0)
; #define G8_MMA(ai, bj, At, Bt) do { __builtin_amdgcn_s_setprio(1); _Pragma("unroll") for (int m = 0; m < 4; ++m) _Pragma("unroll") for (int n = 0; n < 2; ++n) _Pragma("unroll") for (int k = 0; k < 2; ++k) \
;         acc[ai][bj][m][n] = __builtin_amdgcn_mfma_f32_16x16x32_bf16(Bt[n][k], At[m][k], acc[ai][bj][m][n], 0, 0, 0); __builtin_amdgcn_s_setprio(0); } while (0)
; #define G8_WAIT_V(n) asm volatile("s_waitcnt vmcnt(" #n ")" ::: "memory")
; #define G8_WAIT_L(n) asm volatile("s_waitcnt lgkmcnt(" #n ")" ::: "memory")
; #define G8_BAR __builtin_amdgcn_s_barrier()
; #define G8_SCHED __builtin_amdgcn_sched_barrier(0)
; template <class Epi, class Sched>
; __device__ __forceinline__ void gemm_phase(LAS unsigned char* lds, const int K, const Sched& S, const Epi& E) {
;     ...
;             G8_BAR; G8_WAIT_L(0); G8_MMA(0, 1, At, B1); G8_BAR;
;             G8_LDA(At, 1, 1); G8_STAGE(G8_SA(1, 0), a3, oc[0]);
;             G8_BAR; G8_WAIT_L(0); G8_MMA(1, 0, At, B0); G8_BAR; G8_SCHED;
;             G8_STAGE(G8_SB(1, 1), b3 + hstep, voffB);
;             G8_WAIT_V(6); G8_BAR; G8_MMA(1, 1, At, B1); G8_BAR;
;         }
	s_waitcnt lgkmcnt(0)
	s_setprio 1
	s_waitcnt lgkmcnt(0)
	v_mfma_f32_16x16x32_bf16 v[118:121], v[216:219], v[168:171], v[118:121]
	v_mfma_f32_16x16x32_bf16 v[114:117], v[224:227], v[168:171], v[114:117]
	v_mfma_f32_16x16x32_bf16 v[102:105], v[216:219], v[176:179], v[102:105]
	v_mfma_f32_16x16x32_bf16 v[98:101], v[224:227], v[176:179], v[98:101]
	v_mfma_f32_16x16x32_bf16 v[86:89], v[216:219], v[184:187], v[86:89]
	v_mfma_f32_16x16x32_bf16 v[82:85], v[224:227], v[184:187], v[82:85]
	v_mfma_f32_16x16x32_bf16 v[70:73], v[216:219], v[192:195], v[70:73]
	v_mfma_f32_16x16x32_bf16 v[66:69], v[224:227], v[192:195], v[66:69]
	v_mfma_f32_16x16x32_bf16 v[118:121], v[220:223], v[172:175], v[118:121]
	v_mfma_f32_16x16x32_bf16 v[114:117], v[228:231], v[172:175], v[114:117]
	v_mfma_f32_16x16x32_bf16 v[102:105], v[220:223], v[180:183], v[102:105]
	v_mfma_f32_16x16x32_bf16 v[98:101], v[228:231], v[180:183], v[98:101]
	v_mfma_f32_16x16x32_bf16 v[86:89], v[220:223], v[188:191], v[86:89]
	v_mfma_f32_16x16x32_bf16 v[82:85], v[228:231], v[188:191], v[82:85]
	v_mfma_f32_16x16x32_bf16 v[70:73], v[220:223], v[196:199], v[70:73]
	v_mfma_f32_16x16x32_bf16 v[66:69], v[228:231], v[196:199], v[66:69]
	s_setprio 0
	s_mov_b32 m0, s48
	v_lshl_add_u64 v[144:145], v[232:233], 0, s[18:19]
	s_barrier
	ds_read_b128 v[168:171], v150 offset:49152
	ds_read_b128 v[172:175], v150 offset:50176
	ds_read_b128 v[176:179], v150 offset:51200
	ds_read_b128 v[180:183], v150 offset:52224
	ds_read_b128 v[184:187], v150 offset:53248
	ds_read_b128 v[188:191], v150 offset:54272
	ds_read_b128 v[192:195], v150 offset:55296
	ds_read_b128 v[196:199], v150 offset:56320
	global_load_lds_dwordx4 v[144:145], off
	v_lshl_add_u64 v[144:145], v[234:235], 0, s[18:19]
	s_mov_b32 m0, s49
	s_nop 0
	global_load_lds_dwordx4 v[144:145], off
	s_barrier
	s_waitcnt lgkmcnt(0)
	s_setprio 1
	s_waitcnt lgkmcnt(0)
	v_mfma_f32_16x16x32_bf16 v[62:65], v[152:155], v[168:171], v[62:65]
	v_mfma_f32_16x16x32_bf16 v[58:61], v[160:163], v[168:171], v[58:61]
	v_mfma_f32_16x16x32_bf16 v[46:49], v[152:155], v[176:179], v[46:49]
	v_mfma_f32_16x16x32_bf16 v[42:45], v[160:163], v[176:179], v[42:45]
	v_mfma_f32_16x16x32_bf16 v[30:33], v[152:155], v[184:187], v[30:33]
	v_mfma_f32_16x16x32_bf16 v[26:29], v[160:163], v[184:187], v[26:29]
	v_mfma_f32_16x16x32_bf16 v[14:17], v[152:155], v[192:195], v[14:17]
	v_mfma_f32_16x16x32_bf16 v[10:13], v[160:163], v[192:195], v[10:13]
	v_mfma_f32_16x16x32_bf16 v[62:65], v[156:159], v[172:175], v[62:65]
	v_mfma_f32_16x16x32_bf16 v[58:61], v[164:167], v[172:175], v[58:61]
	v_mfma_f32_16x16x32_bf16 v[46:49], v[156:159], v[180:183], v[46:49]
	v_mfma_f32_16x16x32_bf16 v[42:45], v[164:167], v[180:183], v[42:45]
	v_mfma_f32_16x16x32_bf16 v[30:33], v[156:159], v[188:191], v[30:33]
	v_mfma_f32_16x16x32_bf16 v[26:29], v[164:167], v[188:191], v[26:29]
	v_mfma_f32_16x16x32_bf16 v[14:17], v[156:159], v[196:199], v[14:17]
	v_mfma_f32_16x16x32_bf16 v[10:13], v[164:167], v[196:199], v[10:13]
	s_setprio 0
	s_barrier
	s_add_i32 s22, s22, s43
	v_lshl_add_u64 v[144:145], v[236:237], 0, s[18:19]
	s_mov_b32 m0, s22
	s_nop 0
	global_load_lds_dwordx4 v[144:145], off
	v_lshl_add_u64 v[144:145], v[238:239], 0, s[18:19]
	s_add_i32 m0, s22, 0x2000
	s_nop 0
	global_load_lds_dwordx4 v[144:145], off
	s_waitcnt vmcnt(6)
	s_barrier
	s_setprio 1
	v_mfma_f32_16x16x32_bf16 v[54:57], v[216:219], v[168:171], v[54:57]
	v_mfma_f32_16x16x32_bf16 v[50:53], v[224:227], v[168:171], v[50:53]
	v_mfma_f32_16x16x32_bf16 v[38:41], v[216:219], v[176:179], v[38:41]
	v_mfma_f32_16x16x32_bf16 v[34:37], v[224:227], v[176:179], v[34:37]
	v_mfma_f32_16x16x32_bf16 v[22:25], v[216:219], v[184:187], v[22:25]
	v_mfma_f32_16x16x32_bf16 v[18:21], v[224:227], v[184:187], v[18:21]
	v_mfma_f32_16x16x32_bf16 v[6:9], v[216:219], v[192:195], v[6:9]
	v_mfma_f32_16x16x32_bf16 v[2:5], v[224:227], v[192:195], v[2:5]
	v_mfma_f32_16x16x32_bf16 v[54:57], v[220:223], v[172:175], v[54:57]
	v_mfma_f32_16x16x32_bf16 v[50:53], v[228:231], v[172:175], v[50:53]
	v_mfma_f32_16x16x32_bf16 v[38:41], v[220:223], v[180:183], v[38:41]
	v_mfma_f32_16x16x32_bf16 v[34:37], v[228:231], v[180:183], v[34:37]
	v_mfma_f32_16x16x32_bf16 v[22:25], v[220:223], v[188:191], v[22:25]
	v_mfma_f32_16x16x32_bf16 v[18:21], v[228:231], v[188:191], v[18:21]
	v_mfma_f32_16x16x32_bf16 v[6:9], v[220:223], v[196:199], v[6:9]
	v_mfma_f32_16x16x32_bf16 v[2:5], v[228:231], v[196:199], v[2:5]
	s_setprio 0
	s_add_u32 s12, s12, 0x100
	s_addc_u32 s13, s13, 0
	s_add_u32 s58, s58, 0x100
	s_addc_u32 s59, s59, 0
	s_cmp_ge_u32 s60, s50
	s_mov_b32 s22, s60
	s_barrier
	s_cbranch_scc0 .LBB0_2252
; __device__ __forceinline__ unsigned cvt_pk_bf16(float lo, float hi) { unsigned r; asm volatile("v_cvt_pk_bf16_f32 %0, %1, %2" : "=v"(r) : "v"(lo), "v"(hi)); return r; }
;     __device__ __forceinline__ void init(f32x4 (&acc)[2][2][4][2], const Unit& u, int wc, int fq) const {
;         const int col0 = u.pn * BM + wc * 32 + 8 * fq;
; #pragma unroll
;         for (int b = 0; b < 2; ++b)
; #pragma unroll
;             for (int n = 0; n < 2; ++n) { const f32x4 bv = *(const f32x4*)(bias + col0 + b * HALF + 4 * n);
;     __device__ __forceinline__ void operator()(const f32x4 (&acc)[2][2][4][2], const Unit& u, int wr, int wc, int fr, int fq) const {
;         const int row0 = u.pm * BM + wr * 64 + fr, col0 = u.pn * BM + wc * 32 + 8 * fq;
; #pragma unroll
;         for (int ai = 0; ai < 2; ++ai)
; #pragma unroll
;             for (int m = 0; m < 4; ++m) { bf16_t* rowp = O + (size_t)(row0 + ai * HALF + m * 16) * ldc + col0;
; #pragma unroll
;                 for (int bj = 0; bj < 2; ++bj) { const f32x4 v0 = acc[ai][bj][m][0], v1 = acc[ai][bj][m][1];
;                     u32x4 w; w[0] = cvt_pk_bf16(v0[0], v0[1]); w[1] = cvt_pk_bf16(v0[2], v0[3]); w[2] = cvt_pk_bf16(v1[0], v1[1]); w[3] = cvt_pk_bf16(v1[2], v1[3]);
;                     *(u32x4*)(rowp + bj * HALF) = w; } }
;     }
	s_nop 0
	s_nop 0
	s_nop 0
	s_nop 0
	s_nop 0
	s_nop 0
	s_nop 0
	v_lshl_add_u32 v152, s56, 8, v147
	v_lshl_or_b32 v144, s57, 8, v149
	v_ashrrev_i32_e32 v153, 31, v152
	v_ashrrev_i32_e32 v145, 31, v144
	v_lshlrev_b64 v[154:155], 11, v[152:153]
	v_lshl_add_u64 v[154:155], s[4:5], 0, v[154:155]
	v_lshlrev_b64 v[156:157], 1, v[144:145]
	v_lshl_add_u64 v[144:145], v[154:155], 0, v[156:157]
	v_cvt_pk_bf16_f32 v126, v126, v127
	v_cvt_pk_bf16_f32 v127, v128, v129
	v_cvt_pk_bf16_f32 v128, v122, v123
	v_cvt_pk_bf16_f32 v129, v124, v125
	global_store_dwordx4 v[144:145], v[126:129], off
	v_cvt_pk_bf16_f32 v118, v118, v119
	v_cvt_pk_bf16_f32 v119, v120, v121
	v_cvt_pk_bf16_f32 v120, v114, v115
	v_or_b32_e32 v114, 16, v152
	v_ashrrev_i32_e32 v115, 31, v114
	v_lshlrev_b64 v[114:115], 11, v[114:115]
	v_lshl_add_u64 v[114:115], s[4:5], 0, v[114:115]
	v_lshl_add_u64 v[114:115], v[114:115], 0, v[156:157]
	v_cvt_pk_bf16_f32 v121, v116, v117
	global_store_dwordx4 v[144:145], v[118:121], off offset:256
	v_cvt_pk_bf16_f32 v110, v110, v111
	v_cvt_pk_bf16_f32 v111, v112, v113
	v_cvt_pk_bf16_f32 v112, v106, v107
	v_cvt_pk_bf16_f32 v113, v108, v109
	global_store_dwordx4 v[114:115], v[110:113], off
	v_cvt_pk_bf16_f32 v102, v102, v103
	v_cvt_pk_bf16_f32 v103, v104, v105
	v_cvt_pk_bf16_f32 v104, v98, v99
	v_or_b32_e32 v98, 32, v152
	v_ashrrev_i32_e32 v99, 31, v98
	v_lshlrev_b64 v[98:99], 11, v[98:99]
	v_lshl_add_u64 v[98:99], s[4:5], 0, v[98:99]
	v_lshl_add_u64 v[98:99], v[98:99], 0, v[156:157]
	v_cvt_pk_bf16_f32 v105, v100, v101
	global_store_dwordx4 v[114:115], v[102:105], off offset:256
	v_cvt_pk_bf16_f32 v94, v94, v95
	v_cvt_pk_bf16_f32 v95, v96, v97
	v_cvt_pk_bf16_f32 v96, v90, v91
	v_cvt_pk_bf16_f32 v97, v92, v93
	global_store_dwordx4 v[98:99], v[94:97], off
	v_cvt_pk_bf16_f32 v86, v86, v87
	v_cvt_pk_bf16_f32 v87, v88, v89
	v_cvt_pk_bf16_f32 v88, v82, v83
	v_or_b32_e32 v82, 48, v152
	v_ashrrev_i32_e32 v83, 31, v82
	v_lshlrev_b64 v[82:83], 11, v[82:83]
	v_lshl_add_u64 v[82:83], s[4:5], 0, v[82:83]
	v_lshl_add_u64 v[82:83], v[82:83], 0, v[156:157]
	s_mov_b64 s[0:1], 0x40000
	v_cvt_pk_bf16_f32 v89, v84, v85
	global_store_dwordx4 v[98:99], v[86:89], off offset:256
	v_cvt_pk_bf16_f32 v78, v78, v79
	v_cvt_pk_bf16_f32 v79, v80, v81
	v_cvt_pk_bf16_f32 v80, v74, v75
	v_cvt_pk_bf16_f32 v81, v76, v77
	global_store_dwordx4 v[82:83], v[78:81], off
	v_cvt_pk_bf16_f32 v70, v70, v71
	v_cvt_pk_bf16_f32 v71, v72, v73
	v_cvt_pk_bf16_f32 v72, v66, v67
	v_cvt_pk_bf16_f32 v73, v68, v69
	global_store_dwordx4 v[82:83], v[70:73], off offset:256
	v_lshl_add_u64 v[66:67], v[144:145], 0, s[0:1]
	v_cvt_pk_bf16_f32 v62, v62, v63
	v_cvt_pk_bf16_f32 v63, v64, v65
	v_cvt_pk_bf16_f32 v64, v58, v59
	v_add_co_u32_e64 v58, s[0:1], s82, v144
	v_cvt_pk_bf16_f32 v65, v60, v61
	s_and_b64 vcc, exec, vcc
	s_nop 0
	v_addc_co_u32_e64 v59, s[0:1], 0, v145, s[0:1]
	s_mov_b64 s[0:1], 0x48000
	global_store_dwordx4 v[58:59], v[62:65], off
	v_cvt_pk_bf16_f32 v54, v54, v55
	v_cvt_pk_bf16_f32 v55, v56, v57
	v_cvt_pk_bf16_f32 v56, v50, v51
	v_lshl_add_u64 v[50:51], v[144:145], 0, s[0:1]
	s_mov_b32 s0, 0x48000
	v_cvt_pk_bf16_f32 v57, v52, v53
	global_store_dwordx4 v[66:67], v[54:57], off offset:256
	v_cvt_pk_bf16_f32 v46, v46, v47
	v_cvt_pk_bf16_f32 v47, v48, v49
	v_cvt_pk_bf16_f32 v48, v42, v43
	v_add_co_u32_e64 v42, s[0:1], s0, v144
	v_cvt_pk_bf16_f32 v49, v44, v45
	s_nop 1
	v_addc_co_u32_e64 v43, s[0:1], 0, v145, s[0:1]
	s_mov_b64 s[0:1], 0x50000
	global_store_dwordx4 v[42:43], v[46:49], off
	v_cvt_pk_bf16_f32 v38, v38, v39
	v_cvt_pk_bf16_f32 v39, v40, v41
	v_cvt_pk_bf16_f32 v40, v34, v35
	v_lshl_add_u64 v[34:35], v[144:145], 0, s[0:1]
	s_mov_b32 s0, 0x50000
	v_cvt_pk_bf16_f32 v41, v36, v37
	global_store_dwordx4 v[50:51], v[38:41], off offset:256
	v_cvt_pk_bf16_f32 v30, v30, v31
	v_cvt_pk_bf16_f32 v31, v32, v33
	v_cvt_pk_bf16_f32 v32, v26, v27
	v_add_co_u32_e64 v26, s[0:1], s0, v144
	v_cvt_pk_bf16_f32 v33, v28, v29
	s_nop 1
	v_addc_co_u32_e64 v27, s[0:1], 0, v145, s[0:1]
	s_mov_b64 s[0:1], 0x58000
	global_store_dwordx4 v[26:27], v[30:33], off
	v_cvt_pk_bf16_f32 v22, v22, v23
	v_cvt_pk_bf16_f32 v23, v24, v25
	v_cvt_pk_bf16_f32 v24, v18, v19
	v_lshl_add_u64 v[18:19], v[144:145], 0, s[0:1]
	s_mov_b32 s0, 0x58000
	v_cvt_pk_bf16_f32 v25, v20, v21
	global_store_dwordx4 v[34:35], v[22:25], off offset:256
	v_cvt_pk_bf16_f32 v14, v14, v15
	v_cvt_pk_bf16_f32 v15, v16, v17
	v_cvt_pk_bf16_f32 v16, v10, v11
	v_add_co_u32_e64 v10, s[0:1], s0, v144
	v_cvt_pk_bf16_f32 v17, v12, v13
	s_nop 1
	v_addc_co_u32_e64 v11, s[0:1], 0, v145, s[0:1]
	global_store_dwordx4 v[10:11], v[14:17], off
	v_cvt_pk_bf16_f32 v6, v6, v7
	v_cvt_pk_bf16_f32 v7, v8, v9
	v_cvt_pk_bf16_f32 v8, v2, v3
	v_cvt_pk_bf16_f32 v9, v4, v5
	s_mov_b64 s[0:1], -1
	global_store_dwordx4 v[18:19], v[6:9], off offset:256
	s_cbranch_vccz .LBB0_2244
	v_lshl_or_b32 v2, s54, 8, v149
	v_ashrrev_i32_e32 v3, 31, v2
	v_lshl_add_u64 v[6:7], v[2:3], 2, s[2:3]
	global_load_dwordx4 v[10:13], v[6:7], off offset:16
	global_load_dwordx4 v[14:17], v[6:7], off
	global_load_dwordx4 v[2:5], v[6:7], off offset:528
	s_nop 0
	global_load_dwordx4 v[6:9], v[6:7], off offset:512
	s_mov_b64 s[0:1], 0
	s_branch .LBB0_2244
